# out-proj epilogue: adjacent 8-byte bf16 H / H*gain stores merged into 16-byte stores (v6 + store merge)
# baseline (speedup 1.0000x reference)
; __device__ __forceinline__ unsigned cvt_pk_bf16(float lo, float hi) { unsigned r; asm volatile("v_cvt_pk_bf16_f32 %0, %1, %2" : "=v"(r) : "v"(lo), "v"(hi)); return r; }
;     __device__ __forceinline__ void operator()(const f32x4 (&acc)[2][2][4][2], const Unit& u, int wr, int wc, int fr, int fq) const {
;         const int row0 = u.pm * BM + wr * 64 + fr, col0 = u.pn * BM + wc * 32 + 8 * fq;
;         f32x4 cs[2][2];
; #pragma unroll
;         for (int bj = 0; bj < 2; ++bj)
; #pragma unroll
;             for (int n = 0; n < 2; ++n) { const u32x4 c = *(const u32x4*)(cmax + col0 + bj * HALF + n * 4);
;                 cs[bj][n] = (f32x4){__uint_as_float(c.x << 16), __uint_as_float(c.y << 16), __uint_as_float(c.z << 16), __uint_as_float(c.w << 16)} * (1.0f / 127.0f); }
; #pragma unroll
;         for (int ai = 0; ai < 2; ++ai)
; #pragma unroll
;             for (int m = 0; m < 4; ++m) { const int row = row0 + ai * HALF + m * 16; const size_t ro = (size_t)row * ldc + col0; float ss = 0.f; const float rs = xs[row];
; #pragma unroll
;                 for (int bj = 0; bj < 2; ++bj)
; #pragma unroll
;                     for (int n = 0; n < 2; ++n) { const i32x4 ia = __builtin_bit_cast(i32x4, acc[ai][bj][m][n]);
;                         const f32x4 af = (f32x4){(float)ia[0], (float)ia[1], (float)ia[2], (float)ia[3]} * rs * cs[bj][n];
;                         f32x4 rv; if constexpr (RB16) { const u32x2 rb = *(const u32x2*)((const bf16_t*)R + ro + bj * HALF + n * 4); rv = (f32x4){__uint_as_float(rb.x << 16), __uint_as_float(rb.x & 0xffff0000u), __uint_as_float(rb.y << 16), __uint_as_float(rb.y & 0xffff0000u)}; }
;                         else rv = *(const f32x4*)((const float*)R + ro + bj * HALF + n * 4);
;                         const f32x4 v = af + rv; { u32x2 hb; hb.x = cvt_pk_bf16(v[0], v[1]); hb.y = cvt_pk_bf16(v[2], v[3]); *(u32x2*)(C + ro + bj * HALF + n * 4) = hb; }
;                         const f32x4 g = *(const f32x4*)(gain + col0 + bj * HALF + n * 4);
;                         u32x2 o; o.x = cvt_pk_bf16(v[0] * g[0], v[1] * g[1]); o.y = cvt_pk_bf16(v[2] * g[2], v[3] * g[3]); *(u32x2*)(HG + ro + bj * HALF + n * 4) = o;
;                         ss += (v[0] * v[0] + v[1] * v[1]) + (v[2] * v[2] + v[3] * v[3]); }
.LBB0_881:
	v_lshl_or_b32 v146, s14, 8, v157
	v_ashrrev_i32_e32 v147, 31, v146
	v_lshl_add_u32 v148, s50, 8, v1
	v_lshlrev_b64 v[166:167], 2, v[146:147]
	v_ashrrev_i32_e32 v149, 31, v148
	v_lshl_add_u64 v[174:175], s[28:29], 0, v[166:167]
	v_lshlrev_b64 v[162:163], 12, v[148:149]
	global_load_dwordx4 v[152:155], v[174:175], off
	v_lshl_add_u64 v[150:151], v[148:149], 2, s[24:25]
	v_lshl_add_u64 v[180:181], v[162:163], 0, v[146:147]
	global_load_dword v178, v[150:151], off
	v_lshl_add_u64 v[182:183], v[180:181], 2, s[10:11]
	global_load_dwordx4 v[162:165], v[182:183], off
	v_cvt_f32_i32_e32 v129, v129
	v_cvt_f32_i32_e32 v128, v128
	v_cvt_f32_i32_e32 v185, v127
	v_cvt_f32_i32_e32 v184, v126
	v_lshlrev_b64 v[180:181], 1, v[180:181]
	v_lshl_add_u64 v[186:187], s[18:19], 0, v[180:181]
	v_lshl_add_u64 v[126:127], s[12:13], 0, v[166:167]
	global_load_dwordx4 v[166:169], v[174:175], off offset:528
	global_load_dwordx4 v[170:173], v[174:175], off offset:16
	s_nop 0
	global_load_dwordx4 v[174:177], v[174:175], off offset:512
	v_lshl_add_u64 v[180:181], s[20:21], 0, v[180:181]
	v_cvt_f32_i32_e32 v125, v125
	v_cvt_f32_i32_e32 v124, v124
	v_cvt_f32_i32_e32 v123, v123
	v_cvt_f32_i32_e32 v122, v122
	v_cvt_f32_i32_e32 v121, v121
	v_cvt_f32_i32_e32 v120, v120
	v_cvt_f32_i32_e32 v119, v119
	v_cvt_f32_i32_e32 v118, v118
	v_cvt_f32_i32_e32 v117, v117
	v_cvt_f32_i32_e32 v116, v116
	v_cvt_f32_i32_e32 v115, v115
	v_cvt_f32_i32_e32 v114, v114
	s_lshl_b32 s50, s14, 2
	s_ashr_i32 s51, s50, 31
	global_load_dwordx4 v[192:195], v[126:127], off
	global_load_dwordx4 v[196:199], v[182:183], off offset:16
	global_load_dwordx4 v[200:203], v[126:127], off offset:16
	global_load_dwordx4 v[204:207], v[182:183], off offset:512
	global_load_dwordx4 v[208:211], v[126:127], off offset:512
	global_load_dwordx4 v[212:215], v[182:183], off offset:528
	global_load_dwordx4 v[216:219], v[126:127], off offset:528
	v_or_b32_e32 v230, 16, v148
	v_ashrrev_i32_e32 v231, 31, v230
	v_lshl_add_u64 v[252:253], v[230:231], 2, s[24:25]
	global_load_dword v250, v[252:253], off
	v_or_b32_e32 v254, 16, v148
	v_ashrrev_i32_e32 v255, 31, v254
	v_lshlrev_b64 v[248:249], 12, v[254:255]
	v_lshl_add_u64 v[230:231], v[248:249], 0, v[146:147]
	v_lshl_add_u64 v[252:253], v[230:231], 2, s[10:11]
	global_load_dwordx4 v[220:223], v[252:253], off
	global_load_dwordx4 v[224:227], v[252:253], off offset:16
	global_load_dwordx4 v[232:235], v[252:253], off offset:512
	global_load_dwordx4 v[236:239], v[252:253], off offset:528
	s_nop 0
	s_waitcnt vmcnt(17)
	v_lshlrev_b32_e32 v152, 16, v152
	v_lshlrev_b32_e32 v153, 16, v153
	v_lshlrev_b32_e32 v154, 16, v154
	v_lshlrev_b32_e32 v155, 16, v155
	s_waitcnt vmcnt(16)
	v_pk_mul_f32 v[184:185], v[178:179], v[184:185] op_sel_hi:[0,1]
	v_pk_mul_f32 v[188:189], v[178:179], v[128:129] op_sel_hi:[0,1]
	v_pk_mul_f32 v[128:129], v[154:155], s[38:39] op_sel_hi:[1,0]
	v_pk_mul_f32 v[152:153], v[152:153], s[38:39] op_sel_hi:[1,0]
	s_waitcnt vmcnt(15)
	v_pk_fma_f32 v[154:155], v[188:189], v[128:129], v[164:165]
	v_pk_fma_f32 v[184:185], v[184:185], v[152:153], v[162:163]
	v_pk_mul_f32 v[188:189], v[178:179], v[122:123] op_sel_hi:[0,1]
	v_cvt_pk_bf16_f32 v240, v184, v185
	v_cvt_pk_bf16_f32 v241, v154, v155
	s_nop 0
	s_nop 0
	s_waitcnt vmcnt(13)
	v_lshlrev_b32_e32 v170, 16, v170
	v_lshlrev_b32_e32 v171, 16, v171
	v_lshlrev_b32_e32 v172, 16, v172
	v_lshlrev_b32_e32 v173, 16, v173
	v_pk_mul_f32 v[190:191], v[178:179], v[124:125] op_sel_hi:[0,1]
	v_pk_mul_f32 v[122:123], v[172:173], s[38:39] op_sel_hi:[1,0]
	v_pk_mul_f32 v[124:125], v[170:171], s[38:39] op_sel_hi:[1,0]
	s_waitcnt vmcnt(12)
	v_lshlrev_b32_e32 v174, 16, v174
	v_lshlrev_b32_e32 v175, 16, v175
	v_lshlrev_b32_e32 v176, 16, v176
	v_lshlrev_b32_e32 v177, 16, v177
	v_lshlrev_b32_e32 v166, 16, v166
	v_lshlrev_b32_e32 v167, 16, v167
	v_lshlrev_b32_e32 v168, 16, v168
	v_lshlrev_b32_e32 v169, 16, v169
	s_nop 0
	s_waitcnt vmcnt(11)
	v_mul_f32_e32 v162, v192, v184
	v_mul_f32_e32 v163, v193, v185
	v_mul_f32_e32 v164, v194, v154
	v_mul_f32_e32 v165, v195, v155
	v_cvt_pk_bf16_f32 v244, v162, v163
	v_cvt_pk_bf16_f32 v245, v164, v165
	s_nop 0
	s_nop 0
	v_mul_f32_e32 v155, v155, v155
	v_fmac_f32_e32 v155, v154, v154
	s_nop 0
	s_waitcnt vmcnt(10)
	v_pk_fma_f32 v[170:171], v[190:191], v[122:123], v[198:199]
	v_pk_fma_f32 v[172:173], v[188:189], v[124:125], v[196:197]
	v_pk_mul_f32 v[188:189], v[178:179], v[118:119] op_sel_hi:[0,1]
	v_cvt_pk_bf16_f32 v242, v172, v173
	v_cvt_pk_bf16_f32 v243, v170, v171
	global_store_dwordx4 v[186:187], v[240:243], off
	s_nop 0
	v_pk_mul_f32 v[190:191], v[178:179], v[120:121] op_sel_hi:[0,1]
	v_pk_mul_f32 v[118:119], v[176:177], s[38:39] op_sel_hi:[1,0]
	v_pk_mul_f32 v[120:121], v[174:175], s[38:39] op_sel_hi:[1,0]
	s_nop 0
	s_waitcnt vmcnt(10)
	v_mul_f32_e32 v162, v172, v200
	v_mul_f32_e32 v163, v173, v201
	v_mul_f32_e32 v164, v170, v202
	v_mul_f32_e32 v165, v171, v203
	v_cvt_pk_bf16_f32 v246, v162, v163
	v_cvt_pk_bf16_f32 v247, v164, v165
	global_store_dwordx4 v[180:181], v[244:247], off
	s_nop 0
	v_mul_f32_e32 v171, v171, v171
	v_fmac_f32_e32 v171, v170, v170
	s_nop 0
	s_waitcnt vmcnt(10)
	v_pk_fma_f32 v[174:175], v[190:191], v[118:119], v[206:207]
	v_pk_fma_f32 v[176:177], v[188:189], v[120:121], v[204:205]
	v_mul_f32_e32 v170, v175, v175
	v_cvt_pk_bf16_f32 v240, v176, v177
	v_cvt_pk_bf16_f32 v241, v174, v175
	s_nop 0
	s_nop 0
	v_fmac_f32_e32 v170, v174, v174
	s_nop 0
	s_waitcnt vmcnt(9)
; __device__ __forceinline__ unsigned cvt_pk_bf16(float lo, float hi) { unsigned r; asm volatile("v_cvt_pk_bf16_f32 %0, %1, %2" : "=v"(r) : "v"(lo), "v"(hi)); return r; }
;     __device__ __forceinline__ void operator()(const f32x4 (&acc)[2][2][4][2], const Unit& u, int wr, int wc, int fr, int fq) const {
;     ...
;             for (int m = 0; m < 4; ++m) { const int row = row0 + ai * HALF + m * 16; const size_t ro = (size_t)row * ldc + col0; float ss = 0.f; const float rs = xs[row];
; #pragma unroll
;                 for (int bj = 0; bj < 2; ++bj)
; #pragma unroll
;                     for (int n = 0; n < 2; ++n) { const i32x4 ia = __builtin_bit_cast(i32x4, acc[ai][bj][m][n]);
;                         const f32x4 af = (f32x4){(float)ia[0], (float)ia[1], (float)ia[2], (float)ia[3]} * rs * cs[bj][n];
;                         f32x4 rv; if constexpr (RB16) { const u32x2 rb = *(const u32x2*)((const bf16_t*)R + ro + bj * HALF + n * 4); rv = (f32x4){__uint_as_float(rb.x << 16), __uint_as_float(rb.x & 0xffff0000u), __uint_as_float(rb.y << 16), __uint_as_float(rb.y & 0xffff0000u)}; }
;                         else rv = *(const f32x4*)((const float*)R + ro + bj * HALF + n * 4);
;                         const f32x4 v = af + rv; { u32x2 hb; hb.x = cvt_pk_bf16(v[0], v[1]); hb.y = cvt_pk_bf16(v[2], v[3]); *(u32x2*)(C + ro + bj * HALF + n * 4) = hb; }
;                         const f32x4 g = *(const f32x4*)(gain + col0 + bj * HALF + n * 4);
;                         u32x2 o; o.x = cvt_pk_bf16(v[0] * g[0], v[1] * g[1]); o.y = cvt_pk_bf16(v[2] * g[2], v[3] * g[3]); *(u32x2*)(HG + ro + bj * HALF + n * 4) = o;
;                         ss += (v[0] * v[0] + v[1] * v[1]) + (v[2] * v[2] + v[3] * v[3]); }
;                 ss += __shfl_xor(ss, 16); ss += __shfl_xor(ss, 32);
;                 if (fq == 0) SS[(size_t)row * 64 + u.pn * 4 + wc] = ss; }
	v_mul_f32_e32 v162, v176, v208
	v_mul_f32_e32 v163, v177, v209
	v_mul_f32_e32 v164, v174, v210
	v_mul_f32_e32 v165, v175, v211
	v_cvt_pk_bf16_f32 v244, v162, v163
	v_cvt_pk_bf16_f32 v245, v164, v165
	s_nop 0
	s_nop 0
	v_pk_mul_f32 v[182:183], v[178:179], v[114:115] op_sel_hi:[0,1]
	v_pk_mul_f32 v[178:179], v[178:179], v[116:117] op_sel_hi:[0,1]
	v_pk_mul_f32 v[114:115], v[168:169], s[38:39] op_sel_hi:[1,0]
	v_pk_mul_f32 v[116:117], v[166:167], s[38:39] op_sel_hi:[1,0]
	s_nop 0
	s_waitcnt vmcnt(8)
	v_pk_fma_f32 v[168:169], v[178:179], v[114:115], v[214:215]
	v_pk_fma_f32 v[178:179], v[182:183], v[116:117], v[212:213]
	v_mul_f32_e32 v183, v185, v185
	v_cvt_pk_bf16_f32 v242, v178, v179
	v_cvt_pk_bf16_f32 v243, v168, v169
	global_store_dwordx4 v[186:187], v[240:243], off offset:256
	s_nop 0
	v_fmac_f32_e32 v183, v184, v184
	v_add_f32_e32 v154, v183, v155
	v_mul_f32_e32 v155, v173, v173
	v_fmac_f32_e32 v155, v172, v172
	v_add_f32_e32 v155, v155, v171
	v_add_f32_e32 v154, v154, v155
	v_mul_f32_e32 v155, v177, v177
	v_fmac_f32_e32 v155, v176, v176
	v_and_b32_e32 v163, 64, v161
	v_add_f32_e32 v155, v155, v170
	v_xor_b32_e32 v162, 16, v161
	v_add_u32_e32 v163, 64, v163
	v_add_f32_e32 v154, v154, v155
	v_mul_f32_e32 v155, v179, v179
	v_mul_f32_e32 v170, v169, v169
	v_cmp_lt_i32_e32 vcc, v162, v163
	v_fmac_f32_e32 v155, v178, v178
	v_fmac_f32_e32 v170, v168, v168
	v_cndmask_b32_e32 v162, v161, v162, vcc
	v_add_f32_e32 v155, v155, v170
	v_lshlrev_b32_e32 v162, 2, v162
	v_add_f32_e32 v154, v154, v155
	ds_bpermute_b32 v155, v162, v154
	v_xor_b32_e32 v182, 32, v161
	v_cmp_lt_i32_e32 vcc, v182, v163
	s_waitcnt lgkmcnt(0)
	v_add_f32_e32 v154, v154, v155
	v_cndmask_b32_e32 v163, v161, v182, vcc
	v_lshlrev_b32_e32 v163, 2, v163
	ds_bpermute_b32 v155, v163, v154
	s_nop 0
	s_waitcnt vmcnt(8)
	v_mul_f32_e32 v164, v178, v216
	v_mul_f32_e32 v165, v179, v217
	v_mul_f32_e32 v166, v168, v218
	v_mul_f32_e32 v167, v169, v219
	v_cvt_pk_bf16_f32 v246, v164, v165
	v_cvt_pk_bf16_f32 v247, v166, v167
	global_store_dwordx4 v[180:181], v[244:247], off offset:256
	s_and_saveexec_b64 s[52:53], s[4:5]
	s_cbranch_execz .LBB0_883
	s_waitcnt lgkmcnt(0)
	v_add_f32_e32 v164, v154, v155
	v_lshlrev_b64 v[154:155], 8, v[148:149]
	v_lshl_add_u64 v[154:155], s[22:23], 0, v[154:155]
	v_lshl_add_u64 v[154:155], s[50:51], 2, v[154:155]
	s_lshl_b32 s14, s66, 2
	v_lshl_add_u64 v[154:155], v[154:155], 0, s[14:15]
	global_store_dword v[154:155], v164, off
.LBB0_883:
	s_or_b64 exec, exec, s[52:53]
	v_or_b32_e32 v254, 32, v148
	v_ashrrev_i32_e32 v255, 31, v254
	v_lshl_add_u64 v[248:249], v[254:255], 2, s[24:25]
	global_load_dword v212, v[248:249], off
	v_or_b32_e32 v230, 32, v148
	v_ashrrev_i32_e32 v231, 31, v230
	v_lshlrev_b64 v[252:253], 12, v[230:231]
	v_lshl_add_u64 v[254:255], v[252:253], 0, v[146:147]
	v_lshl_add_u64 v[248:249], v[254:255], 2, s[10:11]
	global_load_dwordx4 v[240:243], v[248:249], off
	global_load_dwordx4 v[244:247], v[248:249], off offset:16
	global_load_dwordx4 v[196:199], v[248:249], off offset:512
	global_load_dwordx4 v[204:207], v[248:249], off offset:528
	v_or_b32_e32 v154, 16, v148
	s_waitcnt lgkmcnt(0)
	v_ashrrev_i32_e32 v155, 31, v154
	v_lshlrev_b64 v[164:165], 12, v[154:155]
	v_lshl_add_u64 v[168:169], v[164:165], 0, v[146:147]
	v_lshl_add_u64 v[164:165], v[154:155], 2, s[24:25]
	s_nop 0
	v_lshl_add_u64 v[172:173], v[168:169], 2, s[10:11]
	s_nop 0
	v_cvt_f32_i32_e32 v113, v113
	v_cvt_f32_i32_e32 v111, v111
	v_cvt_f32_i32_e32 v110, v110
	v_cvt_f32_i32_e32 v112, v112
	v_lshlrev_b64 v[168:169], 1, v[168:169]
	v_lshl_add_u64 v[174:175], s[18:19], 0, v[168:169]
	v_lshl_add_u64 v[168:169], s[20:21], 0, v[168:169]
	v_cvt_f32_i32_e32 v109, v109
	v_cvt_f32_i32_e32 v107, v107
	v_cvt_f32_i32_e32 v106, v106
	v_cvt_f32_i32_e32 v108, v108
	v_cvt_f32_i32_e32 v105, v105
	v_cvt_f32_i32_e32 v103, v103
	v_cvt_f32_i32_e32 v102, v102
	v_cvt_f32_i32_e32 v104, v104
	v_cvt_f32_i32_e32 v101, v101
	v_cvt_f32_i32_e32 v99, v99
	v_cvt_f32_i32_e32 v98, v98
	v_cvt_f32_i32_e32 v100, v100
	s_nop 0
	s_waitcnt vmcnt(13)
	v_pk_mul_f32 v[110:111], v[250:251], v[110:111] op_sel_hi:[0,1]
	v_pk_mul_f32 v[112:113], v[250:251], v[112:113] op_sel_hi:[0,1]
	s_nop 0
	s_waitcnt vmcnt(12)
	v_pk_fma_f32 v[166:167], v[128:129], v[112:113], v[222:223]
	v_pk_fma_f32 v[164:165], v[152:153], v[110:111], v[220:221]
	v_pk_mul_f32 v[106:107], v[250:251], v[106:107] op_sel_hi:[0,1]
	v_cvt_pk_bf16_f32 v176, v164, v165
	v_cvt_pk_bf16_f32 v177, v166, v167
	s_nop 0
	s_nop 0
	v_pk_mul_f32 v[108:109], v[250:251], v[108:109] op_sel_hi:[0,1]
	v_pk_mul_f32 v[102:103], v[250:251], v[102:103] op_sel_hi:[0,1]
	v_pk_mul_f32 v[104:105], v[250:251], v[104:105] op_sel_hi:[0,1]
	v_pk_mul_f32 v[98:99], v[250:251], v[98:99] op_sel_hi:[0,1]
	v_pk_mul_f32 v[100:101], v[250:251], v[100:101] op_sel_hi:[0,1]
	s_nop 0
	v_mul_f32_e32 v110, v192, v164
	v_mul_f32_e32 v111, v193, v165
	v_mul_f32_e32 v112, v194, v166
	v_mul_f32_e32 v113, v195, v167
	v_cvt_pk_bf16_f32 v180, v110, v111
	v_cvt_pk_bf16_f32 v181, v112, v113
	s_nop 0
	s_nop 0
	s_nop 0
	s_waitcnt vmcnt(11)
	v_pk_fma_f32 v[112:113], v[122:123], v[108:109], v[226:227]
	v_pk_fma_f32 v[110:111], v[124:125], v[106:107], v[224:225]
	s_nop 0
	v_cvt_pk_bf16_f32 v178, v110, v111
	v_cvt_pk_bf16_f32 v179, v112, v113
	global_store_dwordx4 v[174:175], v[176:179], off
	s_nop 0
	s_nop 0
	v_mul_f32_e32 v106, v110, v200
	v_mul_f32_e32 v107, v111, v201
	v_mul_f32_e32 v108, v112, v202
	v_mul_f32_e32 v109, v113, v203
	v_cvt_pk_bf16_f32 v182, v106, v107
	v_cvt_pk_bf16_f32 v183, v108, v109
	global_store_dwordx4 v[168:169], v[180:183], off
	s_nop 0
	s_nop 0
	s_waitcnt vmcnt(12)
; __device__ __forceinline__ unsigned cvt_pk_bf16(float lo, float hi) { unsigned r; asm volatile("v_cvt_pk_bf16_f32 %0, %1, %2" : "=v"(r) : "v"(lo), "v"(hi)); return r; }
;     __device__ __forceinline__ void operator()(const f32x4 (&acc)[2][2][4][2], const Unit& u, int wr, int wc, int fr, int fq) const {
;     ...
;             for (int m = 0; m < 4; ++m) { const int row = row0 + ai * HALF + m * 16; const size_t ro = (size_t)row * ldc + col0; float ss = 0.f; const float rs = xs[row];
; #pragma unroll
;                 for (int bj = 0; bj < 2; ++bj)
; #pragma unroll
;                     for (int n = 0; n < 2; ++n) { const i32x4 ia = __builtin_bit_cast(i32x4, acc[ai][bj][m][n]);
;                         const f32x4 af = (f32x4){(float)ia[0], (float)ia[1], (float)ia[2], (float)ia[3]} * rs * cs[bj][n];
;                         f32x4 rv; if constexpr (RB16) { const u32x2 rb = *(const u32x2*)((const bf16_t*)R + ro + bj * HALF + n * 4); rv = (f32x4){__uint_as_float(rb.x << 16), __uint_as_float(rb.x & 0xffff0000u), __uint_as_float(rb.y << 16), __uint_as_float(rb.y & 0xffff0000u)}; }
;                         else rv = *(const f32x4*)((const float*)R + ro + bj * HALF + n * 4);
;                         const f32x4 v = af + rv; { u32x2 hb; hb.x = cvt_pk_bf16(v[0], v[1]); hb.y = cvt_pk_bf16(v[2], v[3]); *(u32x2*)(C + ro + bj * HALF + n * 4) = hb; }
;                         const f32x4 g = *(const f32x4*)(gain + col0 + bj * HALF + n * 4);
;                         u32x2 o; o.x = cvt_pk_bf16(v[0] * g[0], v[1] * g[1]); o.y = cvt_pk_bf16(v[2] * g[2], v[3] * g[3]); *(u32x2*)(HG + ro + bj * HALF + n * 4) = o;
;                         ss += (v[0] * v[0] + v[1] * v[1]) + (v[2] * v[2] + v[3] * v[3]); }
;                 ss += __shfl_xor(ss, 16); ss += __shfl_xor(ss, 32);
;                 if (fq == 0) SS[(size_t)row * 64 + u.pn * 4 + wc] = ss; }
	v_pk_fma_f32 v[108:109], v[118:119], v[104:105], v[234:235]
	v_pk_fma_f32 v[106:107], v[120:121], v[102:103], v[232:233]
	s_nop 0
	v_cvt_pk_bf16_f32 v176, v106, v107
	v_cvt_pk_bf16_f32 v177, v108, v109
	s_nop 0
	s_nop 0
	s_nop 0
	v_mul_f32_e32 v102, v106, v208
	v_mul_f32_e32 v103, v107, v209
	v_mul_f32_e32 v104, v108, v210
	v_mul_f32_e32 v105, v109, v211
	v_cvt_pk_bf16_f32 v180, v102, v103
	v_cvt_pk_bf16_f32 v181, v104, v105
	s_nop 0
	s_nop 0
	s_nop 0
	s_waitcnt vmcnt(11)
	v_pk_fma_f32 v[104:105], v[114:115], v[100:101], v[238:239]
	v_pk_fma_f32 v[170:171], v[116:117], v[98:99], v[236:237]
	s_nop 0
	v_cvt_pk_bf16_f32 v178, v170, v171
	v_cvt_pk_bf16_f32 v179, v104, v105
	global_store_dwordx4 v[174:175], v[176:179], off offset:256
	s_nop 0
	v_mul_f32_e32 v98, v165, v165
	v_mul_f32_e32 v99, v167, v167
	v_fmac_f32_e32 v98, v164, v164
	v_fmac_f32_e32 v99, v166, v166
	v_add_f32_e32 v98, v98, v99
	v_mul_f32_e32 v99, v111, v111
	v_mul_f32_e32 v111, v113, v113
	v_fmac_f32_e32 v99, v110, v110
	v_fmac_f32_e32 v111, v112, v112
	v_add_f32_e32 v99, v99, v111
	v_add_f32_e32 v98, v98, v99
	v_mul_f32_e32 v99, v107, v107
	v_mul_f32_e32 v107, v109, v109
	v_fmac_f32_e32 v99, v106, v106
	v_fmac_f32_e32 v107, v108, v108
	v_add_f32_e32 v99, v99, v107
	v_add_f32_e32 v98, v98, v99
	v_mul_f32_e32 v99, v171, v171
	v_mul_f32_e32 v106, v105, v105
	v_fmac_f32_e32 v99, v170, v170
	v_fmac_f32_e32 v106, v104, v104
	v_add_f32_e32 v99, v99, v106
	v_add_f32_e32 v98, v98, v99
	ds_bpermute_b32 v99, v162, v98
	s_waitcnt lgkmcnt(0)
	v_add_f32_e32 v98, v98, v99
	ds_bpermute_b32 v99, v163, v98
	s_nop 0
	v_mul_f32_e32 v100, v170, v216
	v_mul_f32_e32 v101, v171, v217
	v_mul_f32_e32 v102, v104, v218
	v_mul_f32_e32 v103, v105, v219
	v_cvt_pk_bf16_f32 v182, v100, v101
	v_cvt_pk_bf16_f32 v183, v102, v103
	global_store_dwordx4 v[168:169], v[180:183], off offset:256
	s_and_saveexec_b64 s[52:53], s[4:5]
	s_cbranch_execz .LBB0_885
	s_waitcnt lgkmcnt(0)
	v_add_f32_e32 v100, v98, v99
	v_lshlrev_b64 v[98:99], 8, v[154:155]
	v_lshl_add_u64 v[98:99], s[22:23], 0, v[98:99]
	v_lshl_add_u64 v[98:99], s[50:51], 2, v[98:99]
	s_lshl_b32 s14, s66, 2
	v_lshl_add_u64 v[98:99], v[98:99], 0, s[14:15]
	global_store_dword v[98:99], v100, off
.LBB0_885:
	s_or_b64 exec, exec, s[52:53]
	v_or_b32_e32 v230, 48, v148
	v_ashrrev_i32_e32 v231, 31, v230
	v_lshl_add_u64 v[252:253], v[230:231], 2, s[24:25]
	global_load_dword v214, v[252:253], off
	v_or_b32_e32 v254, 48, v148
	v_ashrrev_i32_e32 v255, 31, v254
	v_lshlrev_b64 v[248:249], 12, v[254:255]
	v_lshl_add_u64 v[230:231], v[248:249], 0, v[146:147]
	v_lshl_add_u64 v[252:253], v[230:231], 2, s[10:11]
	global_load_dwordx4 v[220:223], v[252:253], off
	global_load_dwordx4 v[224:227], v[252:253], off offset:16
	global_load_dwordx4 v[232:235], v[252:253], off offset:512
	global_load_dwordx4 v[236:239], v[252:253], off offset:528
	v_or_b32_e32 v98, 32, v148
	s_waitcnt lgkmcnt(0)
	v_ashrrev_i32_e32 v99, 31, v98
	v_lshlrev_b64 v[100:101], 12, v[98:99]
	v_lshl_add_u64 v[104:105], v[100:101], 0, v[146:147]
	v_lshl_add_u64 v[100:101], v[98:99], 2, s[24:25]
	s_nop 0
	v_lshl_add_u64 v[108:109], v[104:105], 2, s[10:11]
	s_nop 0
	v_cvt_f32_i32_e32 v97, v97
	v_cvt_f32_i32_e32 v95, v95
	v_cvt_f32_i32_e32 v94, v94
	v_cvt_f32_i32_e32 v96, v96
	v_lshlrev_b64 v[104:105], 1, v[104:105]
	v_lshl_add_u64 v[110:111], s[18:19], 0, v[104:105]
	v_lshl_add_u64 v[104:105], s[20:21], 0, v[104:105]
	v_cvt_f32_i32_e32 v93, v93
	v_cvt_f32_i32_e32 v91, v91
	v_cvt_f32_i32_e32 v90, v90
	v_cvt_f32_i32_e32 v92, v92
	v_cvt_f32_i32_e32 v89, v89
	v_cvt_f32_i32_e32 v87, v87
	v_cvt_f32_i32_e32 v86, v86
	v_cvt_f32_i32_e32 v88, v88
	v_cvt_f32_i32_e32 v85, v85
	v_cvt_f32_i32_e32 v83, v83
	v_cvt_f32_i32_e32 v82, v82
	v_cvt_f32_i32_e32 v84, v84
	s_nop 0
	s_waitcnt vmcnt(13)
	v_pk_mul_f32 v[94:95], v[212:213], v[94:95] op_sel_hi:[0,1]
	v_pk_mul_f32 v[96:97], v[212:213], v[96:97] op_sel_hi:[0,1]
	s_nop 0
	s_waitcnt vmcnt(12)
	v_pk_fma_f32 v[102:103], v[128:129], v[96:97], v[242:243]
	v_pk_fma_f32 v[100:101], v[152:153], v[94:95], v[240:241]
	v_pk_mul_f32 v[90:91], v[212:213], v[90:91] op_sel_hi:[0,1]
	v_cvt_pk_bf16_f32 v164, v100, v101
	v_cvt_pk_bf16_f32 v165, v102, v103
	s_nop 0
	s_nop 0
	v_pk_mul_f32 v[92:93], v[212:213], v[92:93] op_sel_hi:[0,1]
	v_pk_mul_f32 v[86:87], v[212:213], v[86:87] op_sel_hi:[0,1]
	v_pk_mul_f32 v[88:89], v[212:213], v[88:89] op_sel_hi:[0,1]
	v_pk_mul_f32 v[82:83], v[212:213], v[82:83] op_sel_hi:[0,1]
	v_pk_mul_f32 v[84:85], v[212:213], v[84:85] op_sel_hi:[0,1]
	s_nop 0
	v_mul_f32_e32 v94, v192, v100
	v_mul_f32_e32 v95, v193, v101
	v_mul_f32_e32 v96, v194, v102
	v_mul_f32_e32 v97, v195, v103
	v_cvt_pk_bf16_f32 v168, v94, v95
	v_cvt_pk_bf16_f32 v169, v96, v97
	s_nop 0
	s_nop 0
	s_nop 0
	s_waitcnt vmcnt(11)
	v_pk_fma_f32 v[96:97], v[122:123], v[92:93], v[246:247]
	v_pk_fma_f32 v[94:95], v[124:125], v[90:91], v[244:245]
	s_nop 0
	v_cvt_pk_bf16_f32 v166, v94, v95
	v_cvt_pk_bf16_f32 v167, v96, v97
	global_store_dwordx4 v[110:111], v[164:167], off
	s_nop 0
	s_nop 0
	v_mul_f32_e32 v90, v94, v200
	v_mul_f32_e32 v91, v95, v201
	v_mul_f32_e32 v92, v96, v202
	v_mul_f32_e32 v93, v97, v203
	v_cvt_pk_bf16_f32 v170, v90, v91
	v_cvt_pk_bf16_f32 v171, v92, v93
	global_store_dwordx4 v[104:105], v[168:171], off
	s_nop 0
	s_nop 0
	s_waitcnt vmcnt(12)
	v_pk_fma_f32 v[92:93], v[118:119], v[88:89], v[198:199]
	v_pk_fma_f32 v[90:91], v[120:121], v[86:87], v[196:197]
	s_nop 0
	v_cvt_pk_bf16_f32 v164, v90, v91
	v_cvt_pk_bf16_f32 v165, v92, v93
	s_nop 0
	s_nop 0
	s_nop 0
	v_mul_f32_e32 v86, v90, v208
	v_mul_f32_e32 v87, v91, v209
	v_mul_f32_e32 v88, v92, v210
	v_mul_f32_e32 v89, v93, v211
	v_cvt_pk_bf16_f32 v168, v86, v87
	v_cvt_pk_bf16_f32 v169, v88, v89
	s_nop 0
	s_nop 0
	s_nop 0
	s_waitcnt vmcnt(11)
; __device__ __forceinline__ unsigned cvt_pk_bf16(float lo, float hi) { unsigned r; asm volatile("v_cvt_pk_bf16_f32 %0, %1, %2" : "=v"(r) : "v"(lo), "v"(hi)); return r; }
;     __device__ __forceinline__ void operator()(const f32x4 (&acc)[2][2][4][2], const Unit& u, int wr, int wc, int fr, int fq) const {
;     ...
;             for (int m = 0; m < 4; ++m) { const int row = row0 + ai * HALF + m * 16; const size_t ro = (size_t)row * ldc + col0; float ss = 0.f; const float rs = xs[row];
; #pragma unroll
;                 for (int bj = 0; bj < 2; ++bj)
; #pragma unroll
;                     for (int n = 0; n < 2; ++n) { const i32x4 ia = __builtin_bit_cast(i32x4, acc[ai][bj][m][n]);
;                         const f32x4 af = (f32x4){(float)ia[0], (float)ia[1], (float)ia[2], (float)ia[3]} * rs * cs[bj][n];
;                         f32x4 rv; if constexpr (RB16) { const u32x2 rb = *(const u32x2*)((const bf16_t*)R + ro + bj * HALF + n * 4); rv = (f32x4){__uint_as_float(rb.x << 16), __uint_as_float(rb.x & 0xffff0000u), __uint_as_float(rb.y << 16), __uint_as_float(rb.y & 0xffff0000u)}; }
;                         else rv = *(const f32x4*)((const float*)R + ro + bj * HALF + n * 4);
;                         const f32x4 v = af + rv; { u32x2 hb; hb.x = cvt_pk_bf16(v[0], v[1]); hb.y = cvt_pk_bf16(v[2], v[3]); *(u32x2*)(C + ro + bj * HALF + n * 4) = hb; }
;                         const f32x4 g = *(const f32x4*)(gain + col0 + bj * HALF + n * 4);
;                         u32x2 o; o.x = cvt_pk_bf16(v[0] * g[0], v[1] * g[1]); o.y = cvt_pk_bf16(v[2] * g[2], v[3] * g[3]); *(u32x2*)(HG + ro + bj * HALF + n * 4) = o;
;                         ss += (v[0] * v[0] + v[1] * v[1]) + (v[2] * v[2] + v[3] * v[3]); }
;                 ss += __shfl_xor(ss, 16); ss += __shfl_xor(ss, 32);
;                 if (fq == 0) SS[(size_t)row * 64 + u.pn * 4 + wc] = ss; }
	v_pk_fma_f32 v[88:89], v[114:115], v[84:85], v[206:207]
	v_pk_fma_f32 v[106:107], v[116:117], v[82:83], v[204:205]
	s_nop 0
	v_cvt_pk_bf16_f32 v166, v106, v107
	v_cvt_pk_bf16_f32 v167, v88, v89
	global_store_dwordx4 v[110:111], v[164:167], off offset:256
	s_nop 0
	v_mul_f32_e32 v82, v101, v101
	v_mul_f32_e32 v83, v103, v103
	v_fmac_f32_e32 v82, v100, v100
	v_fmac_f32_e32 v83, v102, v102
	v_add_f32_e32 v82, v82, v83
	v_mul_f32_e32 v83, v95, v95
	v_mul_f32_e32 v95, v97, v97
	v_fmac_f32_e32 v83, v94, v94
	v_fmac_f32_e32 v95, v96, v96
	v_add_f32_e32 v83, v83, v95
	v_add_f32_e32 v82, v82, v83
	v_mul_f32_e32 v83, v91, v91
	v_mul_f32_e32 v91, v93, v93
	v_fmac_f32_e32 v83, v90, v90
	v_fmac_f32_e32 v91, v92, v92
	v_add_f32_e32 v83, v83, v91
	v_add_f32_e32 v82, v82, v83
	v_mul_f32_e32 v83, v107, v107
	v_mul_f32_e32 v90, v89, v89
	v_fmac_f32_e32 v83, v106, v106
	v_fmac_f32_e32 v90, v88, v88
	v_add_f32_e32 v83, v83, v90
	v_add_f32_e32 v82, v82, v83
	ds_bpermute_b32 v83, v162, v82
	s_waitcnt lgkmcnt(0)
	v_add_f32_e32 v82, v82, v83
	ds_bpermute_b32 v83, v163, v82
	s_nop 0
	v_mul_f32_e32 v84, v106, v216
	v_mul_f32_e32 v85, v107, v217
	v_mul_f32_e32 v86, v88, v218
	v_mul_f32_e32 v87, v89, v219
	v_cvt_pk_bf16_f32 v170, v84, v85
	v_cvt_pk_bf16_f32 v171, v86, v87
	global_store_dwordx4 v[104:105], v[168:171], off offset:256
	s_and_saveexec_b64 s[52:53], s[4:5]
	s_cbranch_execz .LBB0_887
	s_waitcnt lgkmcnt(0)
	v_add_f32_e32 v84, v82, v83
	v_lshlrev_b64 v[82:83], 8, v[98:99]
	v_lshl_add_u64 v[82:83], s[22:23], 0, v[82:83]
	v_lshl_add_u64 v[82:83], s[50:51], 2, v[82:83]
	s_lshl_b32 s14, s66, 2
	v_lshl_add_u64 v[82:83], v[82:83], 0, s[14:15]
	global_store_dword v[82:83], v84, off
.LBB0_887:
	s_or_b64 exec, exec, s[52:53]
	global_load_dword v250, v[150:151], off offset:512
	v_add_u32_e32 v254, 0x80, v148
	v_ashrrev_i32_e32 v255, 31, v254
	v_lshlrev_b64 v[248:249], 12, v[254:255]
	v_lshl_add_u64 v[230:231], v[248:249], 0, v[146:147]
	v_lshl_add_u64 v[252:253], v[230:231], 2, s[10:11]
	global_load_dwordx4 v[240:243], v[252:253], off
	global_load_dwordx4 v[244:247], v[252:253], off offset:16
	global_load_dwordx4 v[196:199], v[252:253], off offset:512
	global_load_dwordx4 v[204:207], v[252:253], off offset:528
	v_or_b32_e32 v82, 48, v148
	s_waitcnt lgkmcnt(0)
	v_ashrrev_i32_e32 v83, 31, v82
	v_lshlrev_b64 v[84:85], 12, v[82:83]
	v_lshl_add_u64 v[88:89], v[84:85], 0, v[146:147]
	v_lshl_add_u64 v[84:85], v[82:83], 2, s[24:25]
	s_nop 0
	v_lshl_add_u64 v[92:93], v[88:89], 2, s[10:11]
	s_nop 0
	v_cvt_f32_i32_e32 v81, v81
	v_cvt_f32_i32_e32 v79, v79
	v_cvt_f32_i32_e32 v78, v78
	v_cvt_f32_i32_e32 v80, v80
	v_lshlrev_b64 v[88:89], 1, v[88:89]
	v_lshl_add_u64 v[94:95], s[18:19], 0, v[88:89]
	v_lshl_add_u64 v[88:89], s[20:21], 0, v[88:89]
	v_cvt_f32_i32_e32 v77, v77
	v_cvt_f32_i32_e32 v75, v75
	v_cvt_f32_i32_e32 v74, v74
	v_cvt_f32_i32_e32 v76, v76
	v_cvt_f32_i32_e32 v73, v73
	v_cvt_f32_i32_e32 v71, v71
	v_cvt_f32_i32_e32 v70, v70
	v_cvt_f32_i32_e32 v72, v72
	v_cvt_f32_i32_e32 v69, v69
	v_cvt_f32_i32_e32 v67, v67
	v_cvt_f32_i32_e32 v66, v66
	v_cvt_f32_i32_e32 v68, v68
	s_nop 0
	s_waitcnt vmcnt(13)
	v_pk_mul_f32 v[78:79], v[214:215], v[78:79] op_sel_hi:[0,1]
	v_pk_mul_f32 v[80:81], v[214:215], v[80:81] op_sel_hi:[0,1]
	s_nop 0
	s_waitcnt vmcnt(12)
	v_pk_fma_f32 v[86:87], v[128:129], v[80:81], v[222:223]
	v_pk_fma_f32 v[84:85], v[152:153], v[78:79], v[220:221]
	v_pk_mul_f32 v[74:75], v[214:215], v[74:75] op_sel_hi:[0,1]
	v_cvt_pk_bf16_f32 v96, v84, v85
	v_cvt_pk_bf16_f32 v97, v86, v87
	s_nop 0
	s_nop 0
	v_pk_mul_f32 v[76:77], v[214:215], v[76:77] op_sel_hi:[0,1]
	v_pk_mul_f32 v[70:71], v[214:215], v[70:71] op_sel_hi:[0,1]
	v_pk_mul_f32 v[72:73], v[214:215], v[72:73] op_sel_hi:[0,1]
	v_pk_mul_f32 v[66:67], v[214:215], v[66:67] op_sel_hi:[0,1]
	v_pk_mul_f32 v[68:69], v[214:215], v[68:69] op_sel_hi:[0,1]
	s_nop 0
	v_mul_f32_e32 v78, v192, v84
	v_mul_f32_e32 v79, v193, v85
	v_mul_f32_e32 v80, v194, v86
	v_mul_f32_e32 v81, v195, v87
	v_cvt_pk_bf16_f32 v100, v78, v79
	v_cvt_pk_bf16_f32 v101, v80, v81
	s_nop 0
	s_nop 0
	s_nop 0
	s_waitcnt vmcnt(11)
	v_pk_fma_f32 v[80:81], v[122:123], v[76:77], v[226:227]
	v_pk_fma_f32 v[78:79], v[124:125], v[74:75], v[224:225]
	s_nop 0
	v_cvt_pk_bf16_f32 v98, v78, v79
	v_cvt_pk_bf16_f32 v99, v80, v81
	global_store_dwordx4 v[94:95], v[96:99], off
	s_nop 0
	s_nop 0
	v_mul_f32_e32 v74, v78, v200
	v_mul_f32_e32 v75, v79, v201
	v_mul_f32_e32 v76, v80, v202
	v_mul_f32_e32 v77, v81, v203
	v_cvt_pk_bf16_f32 v102, v74, v75
	v_cvt_pk_bf16_f32 v103, v76, v77
	global_store_dwordx4 v[88:89], v[100:103], off
	s_nop 0
	s_nop 0
	s_waitcnt vmcnt(12)
	v_pk_fma_f32 v[76:77], v[118:119], v[72:73], v[234:235]
	v_pk_fma_f32 v[74:75], v[120:121], v[70:71], v[232:233]
	s_nop 0
	v_cvt_pk_bf16_f32 v96, v74, v75
	v_cvt_pk_bf16_f32 v97, v76, v77
	s_nop 0
	s_nop 0
	s_nop 0
	v_mul_f32_e32 v70, v74, v208
	v_mul_f32_e32 v71, v75, v209
	v_mul_f32_e32 v72, v76, v210
	v_mul_f32_e32 v73, v77, v211
	v_cvt_pk_bf16_f32 v100, v70, v71
	v_cvt_pk_bf16_f32 v101, v72, v73
	s_nop 0
	s_nop 0
	s_nop 0
	s_waitcnt vmcnt(11)
	v_pk_fma_f32 v[72:73], v[114:115], v[68:69], v[238:239]
	v_pk_fma_f32 v[90:91], v[116:117], v[66:67], v[236:237]
	s_nop 0
	v_cvt_pk_bf16_f32 v98, v90, v91
	v_cvt_pk_bf16_f32 v99, v72, v73
	global_store_dwordx4 v[94:95], v[96:99], off offset:256
	s_nop 0
	v_mul_f32_e32 v66, v85, v85
	v_mul_f32_e32 v67, v87, v87
	v_fmac_f32_e32 v66, v84, v84
	v_fmac_f32_e32 v67, v86, v86
	v_add_f32_e32 v66, v66, v67
	v_mul_f32_e32 v67, v79, v79
	v_mul_f32_e32 v79, v81, v81
	v_fmac_f32_e32 v67, v78, v78
	v_fmac_f32_e32 v79, v80, v80
	v_add_f32_e32 v67, v67, v79
	v_add_f32_e32 v66, v66, v67
	v_mul_f32_e32 v67, v75, v75
	v_mul_f32_e32 v75, v77, v77
	v_fmac_f32_e32 v67, v74, v74
	v_fmac_f32_e32 v75, v76, v76
	v_add_f32_e32 v67, v67, v75
	v_add_f32_e32 v66, v66, v67
	v_mul_f32_e32 v67, v91, v91
	v_mul_f32_e32 v74, v73, v73
	v_fmac_f32_e32 v67, v90, v90
	v_fmac_f32_e32 v74, v72, v72
	v_add_f32_e32 v67, v67, v74
	v_add_f32_e32 v66, v66, v67
	ds_bpermute_b32 v67, v162, v66
	s_waitcnt lgkmcnt(0)
	v_add_f32_e32 v66, v66, v67
	ds_bpermute_b32 v67, v163, v66
	s_nop 0
	v_mul_f32_e32 v68, v90, v216
	v_mul_f32_e32 v69, v91, v217
	v_mul_f32_e32 v70, v72, v218
	v_mul_f32_e32 v71, v73, v219
	v_cvt_pk_bf16_f32 v102, v68, v69
	v_cvt_pk_bf16_f32 v103, v70, v71
	global_store_dwordx4 v[88:89], v[100:103], off offset:256
	s_and_saveexec_b64 s[52:53], s[4:5]
	s_cbranch_execz .LBB0_889
	s_waitcnt lgkmcnt(0)
	v_add_f32_e32 v68, v66, v67
	v_lshlrev_b64 v[66:67], 8, v[82:83]
	v_lshl_add_u64 v[66:67], s[22:23], 0, v[66:67]
	v_lshl_add_u64 v[66:67], s[50:51], 2, v[66:67]
	s_lshl_b32 s14, s66, 2
	v_lshl_add_u64 v[66:67], v[66:67], 0, s[14:15]
	global_store_dword v[66:67], v68, off
; __device__ __forceinline__ unsigned cvt_pk_bf16(float lo, float hi) { unsigned r; asm volatile("v_cvt_pk_bf16_f32 %0, %1, %2" : "=v"(r) : "v"(lo), "v"(hi)); return r; }
;     __device__ __forceinline__ void operator()(const f32x4 (&acc)[2][2][4][2], const Unit& u, int wr, int wc, int fr, int fq) const {
;     ...
;             for (int m = 0; m < 4; ++m) { const int row = row0 + ai * HALF + m * 16; const size_t ro = (size_t)row * ldc + col0; float ss = 0.f; const float rs = xs[row];
; #pragma unroll
;                 for (int bj = 0; bj < 2; ++bj)
; #pragma unroll
;                     for (int n = 0; n < 2; ++n) { const i32x4 ia = __builtin_bit_cast(i32x4, acc[ai][bj][m][n]);
;                         const f32x4 af = (f32x4){(float)ia[0], (float)ia[1], (float)ia[2], (float)ia[3]} * rs * cs[bj][n];
;                         f32x4 rv; if constexpr (RB16) { const u32x2 rb = *(const u32x2*)((const bf16_t*)R + ro + bj * HALF + n * 4); rv = (f32x4){__uint_as_float(rb.x << 16), __uint_as_float(rb.x & 0xffff0000u), __uint_as_float(rb.y << 16), __uint_as_float(rb.y & 0xffff0000u)}; }
;                         else rv = *(const f32x4*)((const float*)R + ro + bj * HALF + n * 4);
;                         const f32x4 v = af + rv; { u32x2 hb; hb.x = cvt_pk_bf16(v[0], v[1]); hb.y = cvt_pk_bf16(v[2], v[3]); *(u32x2*)(C + ro + bj * HALF + n * 4) = hb; }
;                         const f32x4 g = *(const f32x4*)(gain + col0 + bj * HALF + n * 4);
;                         u32x2 o; o.x = cvt_pk_bf16(v[0] * g[0], v[1] * g[1]); o.y = cvt_pk_bf16(v[2] * g[2], v[3] * g[3]); *(u32x2*)(HG + ro + bj * HALF + n * 4) = o;
;                         ss += (v[0] * v[0] + v[1] * v[1]) + (v[2] * v[2] + v[3] * v[3]); }
;                 ss += __shfl_xor(ss, 16); ss += __shfl_xor(ss, 32);
;                 if (fq == 0) SS[(size_t)row * 64 + u.pn * 4 + wc] = ss; }
.LBB0_889:
	s_or_b64 exec, exec, s[52:53]
	global_load_dword v212, v[150:151], off offset:576
	v_add_u32_e32 v254, 0x90, v148
	v_ashrrev_i32_e32 v255, 31, v254
	v_lshlrev_b64 v[248:249], 12, v[254:255]
	v_lshl_add_u64 v[230:231], v[248:249], 0, v[146:147]
	v_lshl_add_u64 v[252:253], v[230:231], 2, s[10:11]
	global_load_dwordx4 v[220:223], v[252:253], off
	global_load_dwordx4 v[224:227], v[252:253], off offset:16
	global_load_dwordx4 v[232:235], v[252:253], off offset:512
	global_load_dwordx4 v[236:239], v[252:253], off offset:528
	v_add_u32_e32 v66, 0x80, v148
	s_waitcnt lgkmcnt(0)
	v_ashrrev_i32_e32 v67, 31, v66
	v_lshlrev_b64 v[68:69], 12, v[66:67]
	v_lshl_add_u64 v[72:73], v[68:69], 0, v[146:147]
	s_nop 0
	v_lshl_add_u64 v[76:77], v[72:73], 2, s[10:11]
	s_nop 0
	v_cvt_f32_i32_e32 v65, v65
	v_cvt_f32_i32_e32 v63, v63
	v_cvt_f32_i32_e32 v62, v62
	v_cvt_f32_i32_e32 v64, v64
	v_lshlrev_b64 v[72:73], 1, v[72:73]
	v_lshl_add_u64 v[78:79], s[18:19], 0, v[72:73]
	v_lshl_add_u64 v[72:73], s[20:21], 0, v[72:73]
	v_cvt_f32_i32_e32 v61, v61
	v_cvt_f32_i32_e32 v59, v59
	v_cvt_f32_i32_e32 v58, v58
	v_cvt_f32_i32_e32 v60, v60
	v_cvt_f32_i32_e32 v57, v57
	v_cvt_f32_i32_e32 v55, v55
	v_cvt_f32_i32_e32 v54, v54
	v_cvt_f32_i32_e32 v56, v56
	v_cvt_f32_i32_e32 v53, v53
	v_cvt_f32_i32_e32 v51, v51
	v_cvt_f32_i32_e32 v50, v50
	v_cvt_f32_i32_e32 v52, v52
	s_nop 0
	s_waitcnt vmcnt(13)
	v_pk_mul_f32 v[62:63], v[250:251], v[62:63] op_sel_hi:[0,1]
	v_pk_mul_f32 v[64:65], v[250:251], v[64:65] op_sel_hi:[0,1]
	s_nop 0
	s_waitcnt vmcnt(12)
	v_pk_fma_f32 v[70:71], v[128:129], v[64:65], v[242:243]
	v_pk_fma_f32 v[68:69], v[152:153], v[62:63], v[240:241]
	v_pk_mul_f32 v[58:59], v[250:251], v[58:59] op_sel_hi:[0,1]
	v_cvt_pk_bf16_f32 v80, v68, v69
	v_cvt_pk_bf16_f32 v81, v70, v71
	s_nop 0
	s_nop 0
	v_pk_mul_f32 v[60:61], v[250:251], v[60:61] op_sel_hi:[0,1]
	v_pk_mul_f32 v[54:55], v[250:251], v[54:55] op_sel_hi:[0,1]
	v_pk_mul_f32 v[56:57], v[250:251], v[56:57] op_sel_hi:[0,1]
	v_pk_mul_f32 v[50:51], v[250:251], v[50:51] op_sel_hi:[0,1]
	v_pk_mul_f32 v[52:53], v[250:251], v[52:53] op_sel_hi:[0,1]
	s_nop 0
	v_mul_f32_e32 v62, v192, v68
	v_mul_f32_e32 v63, v193, v69
	v_mul_f32_e32 v64, v194, v70
	v_mul_f32_e32 v65, v195, v71
	v_cvt_pk_bf16_f32 v84, v62, v63
	v_cvt_pk_bf16_f32 v85, v64, v65
	s_nop 0
	s_nop 0
	s_nop 0
	s_waitcnt vmcnt(11)
	v_pk_fma_f32 v[64:65], v[122:123], v[60:61], v[246:247]
	v_pk_fma_f32 v[62:63], v[124:125], v[58:59], v[244:245]
	s_nop 0
	v_cvt_pk_bf16_f32 v82, v62, v63
	v_cvt_pk_bf16_f32 v83, v64, v65
	global_store_dwordx4 v[78:79], v[80:83], off
	s_nop 0
	s_nop 0
	v_mul_f32_e32 v58, v62, v200
	v_mul_f32_e32 v59, v63, v201
	v_mul_f32_e32 v60, v64, v202
	v_mul_f32_e32 v61, v65, v203
	v_cvt_pk_bf16_f32 v86, v58, v59
	v_cvt_pk_bf16_f32 v87, v60, v61
	global_store_dwordx4 v[72:73], v[84:87], off
	s_nop 0
	s_nop 0
	s_waitcnt vmcnt(12)
	v_pk_fma_f32 v[60:61], v[118:119], v[56:57], v[198:199]
	v_pk_fma_f32 v[58:59], v[120:121], v[54:55], v[196:197]
	s_nop 0
	v_cvt_pk_bf16_f32 v80, v58, v59
	v_cvt_pk_bf16_f32 v81, v60, v61
	s_nop 0
	s_nop 0
	s_nop 0
	v_mul_f32_e32 v54, v58, v208
	v_mul_f32_e32 v55, v59, v209
	v_mul_f32_e32 v56, v60, v210
	v_mul_f32_e32 v57, v61, v211
	v_cvt_pk_bf16_f32 v84, v54, v55
	v_cvt_pk_bf16_f32 v85, v56, v57
	s_nop 0
	s_nop 0
	s_nop 0
	s_waitcnt vmcnt(11)
	v_pk_fma_f32 v[56:57], v[114:115], v[52:53], v[206:207]
	v_pk_fma_f32 v[74:75], v[116:117], v[50:51], v[204:205]
	s_nop 0
	v_cvt_pk_bf16_f32 v82, v74, v75
	v_cvt_pk_bf16_f32 v83, v56, v57
	global_store_dwordx4 v[78:79], v[80:83], off offset:256
	s_nop 0
	v_mul_f32_e32 v50, v69, v69
	v_mul_f32_e32 v51, v71, v71
	v_fmac_f32_e32 v50, v68, v68
	v_fmac_f32_e32 v51, v70, v70
	v_add_f32_e32 v50, v50, v51
	v_mul_f32_e32 v51, v63, v63
	v_mul_f32_e32 v63, v65, v65
	v_fmac_f32_e32 v51, v62, v62
	v_fmac_f32_e32 v63, v64, v64
	v_add_f32_e32 v51, v51, v63
	v_add_f32_e32 v50, v50, v51
	v_mul_f32_e32 v51, v59, v59
	v_mul_f32_e32 v59, v61, v61
	v_fmac_f32_e32 v51, v58, v58
	v_fmac_f32_e32 v59, v60, v60
	v_add_f32_e32 v51, v51, v59
	v_add_f32_e32 v50, v50, v51
	v_mul_f32_e32 v51, v75, v75
	v_mul_f32_e32 v58, v57, v57
	v_fmac_f32_e32 v51, v74, v74
	v_fmac_f32_e32 v58, v56, v56
	v_add_f32_e32 v51, v51, v58
	v_add_f32_e32 v50, v50, v51
	ds_bpermute_b32 v51, v162, v50
	s_waitcnt lgkmcnt(0)
	v_add_f32_e32 v50, v50, v51
	ds_bpermute_b32 v51, v163, v50
	s_nop 0
	v_mul_f32_e32 v52, v74, v216
	v_mul_f32_e32 v53, v75, v217
	v_mul_f32_e32 v54, v56, v218
	v_mul_f32_e32 v55, v57, v219
	v_cvt_pk_bf16_f32 v86, v52, v53
	v_cvt_pk_bf16_f32 v87, v54, v55
	global_store_dwordx4 v[72:73], v[84:87], off offset:256
	s_and_saveexec_b64 s[52:53], s[4:5]
	s_cbranch_execz .LBB0_891
	s_waitcnt lgkmcnt(0)
	v_add_f32_e32 v52, v50, v51
	v_lshlrev_b64 v[50:51], 8, v[66:67]
	v_lshl_add_u64 v[50:51], s[22:23], 0, v[50:51]
	v_lshl_add_u64 v[50:51], s[50:51], 2, v[50:51]
	s_lshl_b32 s14, s66, 2
	v_lshl_add_u64 v[50:51], v[50:51], 0, s[14:15]
	global_store_dword v[50:51], v52, off
; __device__ __forceinline__ unsigned cvt_pk_bf16(float lo, float hi) { unsigned r; asm volatile("v_cvt_pk_bf16_f32 %0, %1, %2" : "=v"(r) : "v"(lo), "v"(hi)); return r; }
;     __device__ __forceinline__ void operator()(const f32x4 (&acc)[2][2][4][2], const Unit& u, int wr, int wc, int fr, int fq) const {
;     ...
;             for (int m = 0; m < 4; ++m) { const int row = row0 + ai * HALF + m * 16; const size_t ro = (size_t)row * ldc + col0; float ss = 0.f; const float rs = xs[row];
; #pragma unroll
;                 for (int bj = 0; bj < 2; ++bj)
; #pragma unroll
;                     for (int n = 0; n < 2; ++n) { const i32x4 ia = __builtin_bit_cast(i32x4, acc[ai][bj][m][n]);
;                         const f32x4 af = (f32x4){(float)ia[0], (float)ia[1], (float)ia[2], (float)ia[3]} * rs * cs[bj][n];
;                         f32x4 rv; if constexpr (RB16) { const u32x2 rb = *(const u32x2*)((const bf16_t*)R + ro + bj * HALF + n * 4); rv = (f32x4){__uint_as_float(rb.x << 16), __uint_as_float(rb.x & 0xffff0000u), __uint_as_float(rb.y << 16), __uint_as_float(rb.y & 0xffff0000u)}; }
;                         else rv = *(const f32x4*)((const float*)R + ro + bj * HALF + n * 4);
;                         const f32x4 v = af + rv; { u32x2 hb; hb.x = cvt_pk_bf16(v[0], v[1]); hb.y = cvt_pk_bf16(v[2], v[3]); *(u32x2*)(C + ro + bj * HALF + n * 4) = hb; }
;                         const f32x4 g = *(const f32x4*)(gain + col0 + bj * HALF + n * 4);
;                         u32x2 o; o.x = cvt_pk_bf16(v[0] * g[0], v[1] * g[1]); o.y = cvt_pk_bf16(v[2] * g[2], v[3] * g[3]); *(u32x2*)(HG + ro + bj * HALF + n * 4) = o;
;                         ss += (v[0] * v[0] + v[1] * v[1]) + (v[2] * v[2] + v[3] * v[3]); }
;                 ss += __shfl_xor(ss, 16); ss += __shfl_xor(ss, 32);
;                 if (fq == 0) SS[(size_t)row * 64 + u.pn * 4 + wc] = ss; }
.LBB0_891:
	s_or_b64 exec, exec, s[52:53]
	global_load_dword v214, v[150:151], off offset:640
	v_add_u32_e32 v254, 0xa0, v148
	v_ashrrev_i32_e32 v255, 31, v254
	v_lshlrev_b64 v[248:249], 12, v[254:255]
	v_lshl_add_u64 v[230:231], v[248:249], 0, v[146:147]
	v_lshl_add_u64 v[252:253], v[230:231], 2, s[10:11]
	global_load_dwordx4 v[240:243], v[252:253], off
	global_load_dwordx4 v[244:247], v[252:253], off offset:16
	global_load_dwordx4 v[196:199], v[252:253], off offset:512
	global_load_dwordx4 v[204:207], v[252:253], off offset:528
	v_add_u32_e32 v50, 0x90, v148
	s_waitcnt lgkmcnt(0)
	v_ashrrev_i32_e32 v51, 31, v50
	v_lshlrev_b64 v[52:53], 12, v[50:51]
	v_lshl_add_u64 v[56:57], v[52:53], 0, v[146:147]
	s_nop 0
	v_lshl_add_u64 v[60:61], v[56:57], 2, s[10:11]
	s_nop 0
	v_cvt_f32_i32_e32 v49, v49
	v_cvt_f32_i32_e32 v47, v47
	v_cvt_f32_i32_e32 v46, v46
	v_cvt_f32_i32_e32 v48, v48
	v_lshlrev_b64 v[56:57], 1, v[56:57]
	v_lshl_add_u64 v[62:63], s[18:19], 0, v[56:57]
	v_lshl_add_u64 v[56:57], s[20:21], 0, v[56:57]
	v_cvt_f32_i32_e32 v45, v45
	v_cvt_f32_i32_e32 v43, v43
	v_cvt_f32_i32_e32 v42, v42
	v_cvt_f32_i32_e32 v44, v44
	v_cvt_f32_i32_e32 v41, v41
	v_cvt_f32_i32_e32 v39, v39
	v_cvt_f32_i32_e32 v38, v38
	v_cvt_f32_i32_e32 v40, v40
	v_cvt_f32_i32_e32 v37, v37
	v_cvt_f32_i32_e32 v35, v35
	v_cvt_f32_i32_e32 v34, v34
	v_cvt_f32_i32_e32 v36, v36
	s_nop 0
	s_waitcnt vmcnt(13)
	v_pk_mul_f32 v[46:47], v[212:213], v[46:47] op_sel_hi:[0,1]
	v_pk_mul_f32 v[48:49], v[212:213], v[48:49] op_sel_hi:[0,1]
	s_nop 0
	s_waitcnt vmcnt(12)
	v_pk_fma_f32 v[54:55], v[128:129], v[48:49], v[222:223]
	v_pk_fma_f32 v[52:53], v[152:153], v[46:47], v[220:221]
	v_pk_mul_f32 v[42:43], v[212:213], v[42:43] op_sel_hi:[0,1]
	v_cvt_pk_bf16_f32 v64, v52, v53
	v_cvt_pk_bf16_f32 v65, v54, v55
	s_nop 0
	s_nop 0
	v_pk_mul_f32 v[44:45], v[212:213], v[44:45] op_sel_hi:[0,1]
	v_pk_mul_f32 v[38:39], v[212:213], v[38:39] op_sel_hi:[0,1]
	v_pk_mul_f32 v[40:41], v[212:213], v[40:41] op_sel_hi:[0,1]
	v_pk_mul_f32 v[34:35], v[212:213], v[34:35] op_sel_hi:[0,1]
	v_pk_mul_f32 v[36:37], v[212:213], v[36:37] op_sel_hi:[0,1]
	s_nop 0
	v_mul_f32_e32 v46, v192, v52
	v_mul_f32_e32 v47, v193, v53
	v_mul_f32_e32 v48, v194, v54
	v_mul_f32_e32 v49, v195, v55
	v_cvt_pk_bf16_f32 v68, v46, v47
	v_cvt_pk_bf16_f32 v69, v48, v49
	s_nop 0
	s_nop 0
	s_nop 0
	s_waitcnt vmcnt(11)
	v_pk_fma_f32 v[48:49], v[122:123], v[44:45], v[226:227]
	v_pk_fma_f32 v[46:47], v[124:125], v[42:43], v[224:225]
	s_nop 0
	v_cvt_pk_bf16_f32 v66, v46, v47
	v_cvt_pk_bf16_f32 v67, v48, v49
	global_store_dwordx4 v[62:63], v[64:67], off
	s_nop 0
	s_nop 0
	v_mul_f32_e32 v42, v46, v200
	v_mul_f32_e32 v43, v47, v201
	v_mul_f32_e32 v44, v48, v202
	v_mul_f32_e32 v45, v49, v203
	v_cvt_pk_bf16_f32 v70, v42, v43
	v_cvt_pk_bf16_f32 v71, v44, v45
	global_store_dwordx4 v[56:57], v[68:71], off
	s_nop 0
	s_nop 0
	s_waitcnt vmcnt(12)
	v_pk_fma_f32 v[44:45], v[118:119], v[40:41], v[234:235]
	v_pk_fma_f32 v[42:43], v[120:121], v[38:39], v[232:233]
	s_nop 0
	v_cvt_pk_bf16_f32 v64, v42, v43
	v_cvt_pk_bf16_f32 v65, v44, v45
	s_nop 0
	s_nop 0
	s_nop 0
	v_mul_f32_e32 v38, v42, v208
	v_mul_f32_e32 v39, v43, v209
	v_mul_f32_e32 v40, v44, v210
	v_mul_f32_e32 v41, v45, v211
	v_cvt_pk_bf16_f32 v68, v38, v39
	v_cvt_pk_bf16_f32 v69, v40, v41
	s_nop 0
	s_nop 0
	s_nop 0
	s_waitcnt vmcnt(11)
	v_pk_fma_f32 v[40:41], v[114:115], v[36:37], v[238:239]
	v_pk_fma_f32 v[58:59], v[116:117], v[34:35], v[236:237]
	s_nop 0
	v_cvt_pk_bf16_f32 v66, v58, v59
	v_cvt_pk_bf16_f32 v67, v40, v41
	global_store_dwordx4 v[62:63], v[64:67], off offset:256
	s_nop 0
	v_mul_f32_e32 v34, v53, v53
	v_mul_f32_e32 v35, v55, v55
	v_fmac_f32_e32 v34, v52, v52
	v_fmac_f32_e32 v35, v54, v54
	v_add_f32_e32 v34, v34, v35
	v_mul_f32_e32 v35, v47, v47
	v_mul_f32_e32 v47, v49, v49
	v_fmac_f32_e32 v35, v46, v46
	v_fmac_f32_e32 v47, v48, v48
	v_add_f32_e32 v35, v35, v47
	v_add_f32_e32 v34, v34, v35
	v_mul_f32_e32 v35, v43, v43
	v_mul_f32_e32 v43, v45, v45
	v_fmac_f32_e32 v35, v42, v42
	v_fmac_f32_e32 v43, v44, v44
	v_add_f32_e32 v35, v35, v43
	v_add_f32_e32 v34, v34, v35
	v_mul_f32_e32 v35, v59, v59
	v_mul_f32_e32 v42, v41, v41
	v_fmac_f32_e32 v35, v58, v58
	v_fmac_f32_e32 v42, v40, v40
	v_add_f32_e32 v35, v35, v42
	v_add_f32_e32 v34, v34, v35
	ds_bpermute_b32 v35, v162, v34
	s_waitcnt lgkmcnt(0)
	v_add_f32_e32 v34, v34, v35
	ds_bpermute_b32 v35, v163, v34
	s_nop 0
	v_mul_f32_e32 v36, v58, v216
	v_mul_f32_e32 v37, v59, v217
	v_mul_f32_e32 v38, v40, v218
	v_mul_f32_e32 v39, v41, v219
	v_cvt_pk_bf16_f32 v70, v36, v37
	v_cvt_pk_bf16_f32 v71, v38, v39
	global_store_dwordx4 v[56:57], v[68:71], off offset:256
	s_and_saveexec_b64 s[52:53], s[4:5]
	s_cbranch_execz .LBB0_893
	s_waitcnt lgkmcnt(0)
	v_add_f32_e32 v36, v34, v35
	v_lshlrev_b64 v[34:35], 8, v[50:51]
	v_lshl_add_u64 v[34:35], s[22:23], 0, v[34:35]
	v_lshl_add_u64 v[34:35], s[50:51], 2, v[34:35]
	s_lshl_b32 s14, s66, 2
	v_lshl_add_u64 v[34:35], v[34:35], 0, s[14:15]
	global_store_dword v[34:35], v36, off
; __device__ __forceinline__ unsigned cvt_pk_bf16(float lo, float hi) { unsigned r; asm volatile("v_cvt_pk_bf16_f32 %0, %1, %2" : "=v"(r) : "v"(lo), "v"(hi)); return r; }
;     __device__ __forceinline__ void operator()(const f32x4 (&acc)[2][2][4][2], const Unit& u, int wr, int wc, int fr, int fq) const {
;     ...
;             for (int m = 0; m < 4; ++m) { const int row = row0 + ai * HALF + m * 16; const size_t ro = (size_t)row * ldc + col0; float ss = 0.f; const float rs = xs[row];
; #pragma unroll
;                 for (int bj = 0; bj < 2; ++bj)
; #pragma unroll
;                     for (int n = 0; n < 2; ++n) { const i32x4 ia = __builtin_bit_cast(i32x4, acc[ai][bj][m][n]);
;                         const f32x4 af = (f32x4){(float)ia[0], (float)ia[1], (float)ia[2], (float)ia[3]} * rs * cs[bj][n];
;                         f32x4 rv; if constexpr (RB16) { const u32x2 rb = *(const u32x2*)((const bf16_t*)R + ro + bj * HALF + n * 4); rv = (f32x4){__uint_as_float(rb.x << 16), __uint_as_float(rb.x & 0xffff0000u), __uint_as_float(rb.y << 16), __uint_as_float(rb.y & 0xffff0000u)}; }
;                         else rv = *(const f32x4*)((const float*)R + ro + bj * HALF + n * 4);
;                         const f32x4 v = af + rv; { u32x2 hb; hb.x = cvt_pk_bf16(v[0], v[1]); hb.y = cvt_pk_bf16(v[2], v[3]); *(u32x2*)(C + ro + bj * HALF + n * 4) = hb; }
;                         const f32x4 g = *(const f32x4*)(gain + col0 + bj * HALF + n * 4);
;                         u32x2 o; o.x = cvt_pk_bf16(v[0] * g[0], v[1] * g[1]); o.y = cvt_pk_bf16(v[2] * g[2], v[3] * g[3]); *(u32x2*)(HG + ro + bj * HALF + n * 4) = o;
;                         ss += (v[0] * v[0] + v[1] * v[1]) + (v[2] * v[2] + v[3] * v[3]); }
;                 ss += __shfl_xor(ss, 16); ss += __shfl_xor(ss, 32);
;                 if (fq == 0) SS[(size_t)row * 64 + u.pn * 4 + wc] = ss; }
.LBB0_893:
	s_or_b64 exec, exec, s[52:53]
	global_load_dword v250, v[150:151], off offset:704
	v_add_u32_e32 v254, 0xb0, v148
	v_ashrrev_i32_e32 v255, 31, v254
	v_lshlrev_b64 v[248:249], 12, v[254:255]
	v_lshl_add_u64 v[230:231], v[248:249], 0, v[146:147]
	v_lshl_add_u64 v[252:253], v[230:231], 2, s[10:11]
	global_load_dwordx4 v[220:223], v[252:253], off
	global_load_dwordx4 v[224:227], v[252:253], off offset:16
	global_load_dwordx4 v[232:235], v[252:253], off offset:512
	global_load_dwordx4 v[236:239], v[252:253], off offset:528
	v_add_u32_e32 v34, 0xa0, v148
	s_waitcnt lgkmcnt(0)
	v_ashrrev_i32_e32 v35, 31, v34
	v_lshlrev_b64 v[36:37], 12, v[34:35]
	v_lshl_add_u64 v[40:41], v[36:37], 0, v[146:147]
	s_nop 0
	v_lshl_add_u64 v[44:45], v[40:41], 2, s[10:11]
	s_nop 0
	v_cvt_f32_i32_e32 v33, v33
	v_cvt_f32_i32_e32 v31, v31
	v_cvt_f32_i32_e32 v30, v30
	v_cvt_f32_i32_e32 v32, v32
	v_lshlrev_b64 v[40:41], 1, v[40:41]
	v_lshl_add_u64 v[46:47], s[18:19], 0, v[40:41]
	v_lshl_add_u64 v[40:41], s[20:21], 0, v[40:41]
	v_cvt_f32_i32_e32 v29, v29
	v_cvt_f32_i32_e32 v27, v27
	v_cvt_f32_i32_e32 v26, v26
	v_cvt_f32_i32_e32 v28, v28
	v_cvt_f32_i32_e32 v25, v25
	v_cvt_f32_i32_e32 v23, v23
	v_cvt_f32_i32_e32 v22, v22
	v_cvt_f32_i32_e32 v24, v24
	v_cvt_f32_i32_e32 v21, v21
	v_cvt_f32_i32_e32 v19, v19
	v_cvt_f32_i32_e32 v18, v18
	v_cvt_f32_i32_e32 v20, v20
	s_nop 0
	s_waitcnt vmcnt(13)
	v_pk_mul_f32 v[30:31], v[214:215], v[30:31] op_sel_hi:[0,1]
	v_pk_mul_f32 v[32:33], v[214:215], v[32:33] op_sel_hi:[0,1]
	s_nop 0
	s_waitcnt vmcnt(12)
	v_pk_fma_f32 v[38:39], v[128:129], v[32:33], v[242:243]
	v_pk_fma_f32 v[36:37], v[152:153], v[30:31], v[240:241]
	v_pk_mul_f32 v[26:27], v[214:215], v[26:27] op_sel_hi:[0,1]
	v_cvt_pk_bf16_f32 v48, v36, v37
	v_cvt_pk_bf16_f32 v49, v38, v39
	s_nop 0
	s_nop 0
	v_pk_mul_f32 v[28:29], v[214:215], v[28:29] op_sel_hi:[0,1]
	v_pk_mul_f32 v[22:23], v[214:215], v[22:23] op_sel_hi:[0,1]
	v_pk_mul_f32 v[24:25], v[214:215], v[24:25] op_sel_hi:[0,1]
	v_pk_mul_f32 v[18:19], v[214:215], v[18:19] op_sel_hi:[0,1]
	v_pk_mul_f32 v[20:21], v[214:215], v[20:21] op_sel_hi:[0,1]
	s_nop 0
	v_mul_f32_e32 v30, v192, v36
	v_mul_f32_e32 v31, v193, v37
	v_mul_f32_e32 v32, v194, v38
	v_mul_f32_e32 v33, v195, v39
	v_cvt_pk_bf16_f32 v52, v30, v31
	v_cvt_pk_bf16_f32 v53, v32, v33
	s_nop 0
	s_nop 0
	s_nop 0
	s_waitcnt vmcnt(11)
	v_pk_fma_f32 v[32:33], v[122:123], v[28:29], v[246:247]
	v_pk_fma_f32 v[30:31], v[124:125], v[26:27], v[244:245]
	s_nop 0
	v_cvt_pk_bf16_f32 v50, v30, v31
	v_cvt_pk_bf16_f32 v51, v32, v33
	global_store_dwordx4 v[46:47], v[48:51], off
	s_nop 0
	s_nop 0
	v_mul_f32_e32 v26, v30, v200
	v_mul_f32_e32 v27, v31, v201
	v_mul_f32_e32 v28, v32, v202
	v_mul_f32_e32 v29, v33, v203
	v_cvt_pk_bf16_f32 v54, v26, v27
	v_cvt_pk_bf16_f32 v55, v28, v29
	global_store_dwordx4 v[40:41], v[52:55], off
	s_nop 0
	s_nop 0
	s_waitcnt vmcnt(12)
	v_pk_fma_f32 v[28:29], v[118:119], v[24:25], v[198:199]
	v_pk_fma_f32 v[26:27], v[120:121], v[22:23], v[196:197]
	s_nop 0
	v_cvt_pk_bf16_f32 v48, v26, v27
	v_cvt_pk_bf16_f32 v49, v28, v29
	s_nop 0
	s_nop 0
	s_nop 0
	v_mul_f32_e32 v22, v26, v208
	v_mul_f32_e32 v23, v27, v209
	v_mul_f32_e32 v24, v28, v210
	v_mul_f32_e32 v25, v29, v211
	v_cvt_pk_bf16_f32 v52, v22, v23
	v_cvt_pk_bf16_f32 v53, v24, v25
	s_nop 0
	s_nop 0
	s_nop 0
	s_waitcnt vmcnt(11)
	v_pk_fma_f32 v[24:25], v[114:115], v[20:21], v[206:207]
	v_pk_fma_f32 v[42:43], v[116:117], v[18:19], v[204:205]
	s_nop 0
	v_cvt_pk_bf16_f32 v50, v42, v43
	v_cvt_pk_bf16_f32 v51, v24, v25
	global_store_dwordx4 v[46:47], v[48:51], off offset:256
	s_nop 0
	v_mul_f32_e32 v18, v37, v37
	v_mul_f32_e32 v19, v39, v39
	v_fmac_f32_e32 v18, v36, v36
	v_fmac_f32_e32 v19, v38, v38
	v_add_f32_e32 v18, v18, v19
	v_mul_f32_e32 v19, v31, v31
	v_mul_f32_e32 v31, v33, v33
	v_fmac_f32_e32 v19, v30, v30
	v_fmac_f32_e32 v31, v32, v32
	v_add_f32_e32 v19, v19, v31
	v_add_f32_e32 v18, v18, v19
	v_mul_f32_e32 v19, v27, v27
	v_mul_f32_e32 v27, v29, v29
	v_fmac_f32_e32 v19, v26, v26
	v_fmac_f32_e32 v27, v28, v28
	v_add_f32_e32 v19, v19, v27
	v_add_f32_e32 v18, v18, v19
	v_mul_f32_e32 v19, v43, v43
	v_mul_f32_e32 v26, v25, v25
	v_fmac_f32_e32 v19, v42, v42
	v_fmac_f32_e32 v26, v24, v24
	v_add_f32_e32 v19, v19, v26
	v_add_f32_e32 v18, v18, v19
	ds_bpermute_b32 v19, v162, v18
	s_waitcnt lgkmcnt(0)
	v_add_f32_e32 v18, v18, v19
	ds_bpermute_b32 v19, v163, v18
	s_nop 0
	v_mul_f32_e32 v20, v42, v216
	v_mul_f32_e32 v21, v43, v217
	v_mul_f32_e32 v22, v24, v218
	v_mul_f32_e32 v23, v25, v219
	v_cvt_pk_bf16_f32 v54, v20, v21
	v_cvt_pk_bf16_f32 v55, v22, v23
	global_store_dwordx4 v[40:41], v[52:55], off offset:256
	s_and_saveexec_b64 s[52:53], s[4:5]
	s_cbranch_execz .LBB0_895
	s_waitcnt lgkmcnt(0)
	v_add_f32_e32 v20, v18, v19
	v_lshlrev_b64 v[18:19], 8, v[34:35]
	v_lshl_add_u64 v[18:19], s[22:23], 0, v[18:19]
	v_lshl_add_u64 v[18:19], s[50:51], 2, v[18:19]
	s_lshl_b32 s14, s66, 2
	v_lshl_add_u64 v[18:19], v[18:19], 0, s[14:15]
	global_store_dword v[18:19], v20, off
; __device__ __forceinline__ unsigned cvt_pk_bf16(float lo, float hi) { unsigned r; asm volatile("v_cvt_pk_bf16_f32 %0, %1, %2" : "=v"(r) : "v"(lo), "v"(hi)); return r; }
;     __device__ __forceinline__ void operator()(const f32x4 (&acc)[2][2][4][2], const Unit& u, int wr, int wc, int fr, int fq) const {
;     ...
;             for (int m = 0; m < 4; ++m) { const int row = row0 + ai * HALF + m * 16; const size_t ro = (size_t)row * ldc + col0; float ss = 0.f; const float rs = xs[row];
; #pragma unroll
;                 for (int bj = 0; bj < 2; ++bj)
; #pragma unroll
;                     for (int n = 0; n < 2; ++n) { const i32x4 ia = __builtin_bit_cast(i32x4, acc[ai][bj][m][n]);
;                         const f32x4 af = (f32x4){(float)ia[0], (float)ia[1], (float)ia[2], (float)ia[3]} * rs * cs[bj][n];
;                         f32x4 rv; if constexpr (RB16) { const u32x2 rb = *(const u32x2*)((const bf16_t*)R + ro + bj * HALF + n * 4); rv = (f32x4){__uint_as_float(rb.x << 16), __uint_as_float(rb.x & 0xffff0000u), __uint_as_float(rb.y << 16), __uint_as_float(rb.y & 0xffff0000u)}; }
;                         else rv = *(const f32x4*)((const float*)R + ro + bj * HALF + n * 4);
;                         const f32x4 v = af + rv; { u32x2 hb; hb.x = cvt_pk_bf16(v[0], v[1]); hb.y = cvt_pk_bf16(v[2], v[3]); *(u32x2*)(C + ro + bj * HALF + n * 4) = hb; }
;                         const f32x4 g = *(const f32x4*)(gain + col0 + bj * HALF + n * 4);
;                         u32x2 o; o.x = cvt_pk_bf16(v[0] * g[0], v[1] * g[1]); o.y = cvt_pk_bf16(v[2] * g[2], v[3] * g[3]); *(u32x2*)(HG + ro + bj * HALF + n * 4) = o;
;                         ss += (v[0] * v[0] + v[1] * v[1]) + (v[2] * v[2] + v[3] * v[3]); }
;                 ss += __shfl_xor(ss, 16); ss += __shfl_xor(ss, 32);
;                 if (fq == 0) SS[(size_t)row * 64 + u.pn * 4 + wc] = ss; }
.LBB0_895:
	s_or_b64 exec, exec, s[52:53]
	v_add_u32_e32 v18, 0xb0, v148
	s_waitcnt lgkmcnt(0)
	v_ashrrev_i32_e32 v19, 31, v18
	v_lshlrev_b64 v[20:21], 12, v[18:19]
	v_lshl_add_u64 v[24:25], v[20:21], 0, v[146:147]
	s_nop 0
	v_lshl_add_u64 v[28:29], v[24:25], 2, s[10:11]
	s_nop 0
	v_cvt_f32_i32_e32 v17, v17
	v_cvt_f32_i32_e32 v15, v15
	v_cvt_f32_i32_e32 v14, v14
	v_cvt_f32_i32_e32 v16, v16
	v_lshlrev_b64 v[24:25], 1, v[24:25]
	v_lshl_add_u64 v[30:31], s[18:19], 0, v[24:25]
	v_lshl_add_u64 v[24:25], s[20:21], 0, v[24:25]
	v_cvt_f32_i32_e32 v13, v13
	v_cvt_f32_i32_e32 v11, v11
	v_cvt_f32_i32_e32 v10, v10
	v_cvt_f32_i32_e32 v12, v12
	v_cvt_f32_i32_e32 v9, v9
	v_cvt_f32_i32_e32 v7, v7
	v_cvt_f32_i32_e32 v6, v6
	v_cvt_f32_i32_e32 v8, v8
	v_cvt_f32_i32_e32 v5, v5
	v_cvt_f32_i32_e32 v3, v3
	v_cvt_f32_i32_e32 v2, v2
	v_cvt_f32_i32_e32 v4, v4
	s_nop 0
	s_waitcnt vmcnt(8)
	v_pk_mul_f32 v[14:15], v[250:251], v[14:15] op_sel_hi:[0,1]
	v_pk_mul_f32 v[16:17], v[250:251], v[16:17] op_sel_hi:[0,1]
	s_nop 0
	s_waitcnt vmcnt(7)
	v_pk_fma_f32 v[22:23], v[128:129], v[16:17], v[222:223]
	v_pk_fma_f32 v[20:21], v[152:153], v[14:15], v[220:221]
	v_pk_mul_f32 v[10:11], v[250:251], v[10:11] op_sel_hi:[0,1]
	v_cvt_pk_bf16_f32 v32, v20, v21
	v_cvt_pk_bf16_f32 v33, v22, v23
	s_nop 0
	s_nop 0
	v_pk_mul_f32 v[12:13], v[250:251], v[12:13] op_sel_hi:[0,1]
	v_pk_mul_f32 v[6:7], v[250:251], v[6:7] op_sel_hi:[0,1]
	v_pk_mul_f32 v[8:9], v[250:251], v[8:9] op_sel_hi:[0,1]
	v_pk_mul_f32 v[2:3], v[250:251], v[2:3] op_sel_hi:[0,1]
	v_pk_mul_f32 v[4:5], v[250:251], v[4:5] op_sel_hi:[0,1]
	s_nop 0
	v_mul_f32_e32 v14, v192, v20
	v_mul_f32_e32 v15, v193, v21
	v_mul_f32_e32 v16, v194, v22
	v_mul_f32_e32 v17, v195, v23
	v_cvt_pk_bf16_f32 v36, v14, v15
	v_cvt_pk_bf16_f32 v37, v16, v17
	s_nop 0
	s_nop 0
	s_nop 0
	s_waitcnt vmcnt(6)
	v_pk_fma_f32 v[16:17], v[122:123], v[12:13], v[226:227]
	v_pk_fma_f32 v[14:15], v[124:125], v[10:11], v[224:225]
	s_nop 0
	v_cvt_pk_bf16_f32 v34, v14, v15
	v_cvt_pk_bf16_f32 v35, v16, v17
	global_store_dwordx4 v[30:31], v[32:35], off
	s_nop 0
	s_nop 0
	v_mul_f32_e32 v10, v14, v200
	v_mul_f32_e32 v11, v15, v201
	v_mul_f32_e32 v12, v16, v202
	v_mul_f32_e32 v13, v17, v203
	v_cvt_pk_bf16_f32 v38, v10, v11
	v_cvt_pk_bf16_f32 v39, v12, v13
	global_store_dwordx4 v[24:25], v[36:39], off
	s_nop 0
	s_nop 0
	s_waitcnt vmcnt(7)
	v_pk_fma_f32 v[12:13], v[118:119], v[8:9], v[234:235]
	v_pk_fma_f32 v[10:11], v[120:121], v[6:7], v[232:233]
	s_nop 0
	v_cvt_pk_bf16_f32 v32, v10, v11
	v_cvt_pk_bf16_f32 v33, v12, v13
	s_nop 0
	s_nop 0
	s_nop 0
	v_mul_f32_e32 v6, v10, v208
	v_mul_f32_e32 v7, v11, v209
	v_mul_f32_e32 v8, v12, v210
	v_mul_f32_e32 v9, v13, v211
	v_cvt_pk_bf16_f32 v36, v6, v7
	v_cvt_pk_bf16_f32 v37, v8, v9
	s_nop 0
	s_nop 0
	s_nop 0
	s_waitcnt vmcnt(6)
	v_pk_fma_f32 v[8:9], v[114:115], v[4:5], v[238:239]
	v_pk_fma_f32 v[26:27], v[116:117], v[2:3], v[236:237]
	s_nop 0
	v_cvt_pk_bf16_f32 v34, v26, v27
	v_cvt_pk_bf16_f32 v35, v8, v9
	global_store_dwordx4 v[30:31], v[32:35], off offset:256
	s_nop 0
	v_mul_f32_e32 v2, v21, v21
	v_mul_f32_e32 v3, v23, v23
	v_fmac_f32_e32 v2, v20, v20
	v_fmac_f32_e32 v3, v22, v22
	v_add_f32_e32 v2, v2, v3
	v_mul_f32_e32 v3, v15, v15
	v_mul_f32_e32 v15, v17, v17
	v_fmac_f32_e32 v3, v14, v14
	v_fmac_f32_e32 v15, v16, v16
	v_add_f32_e32 v3, v3, v15
	v_add_f32_e32 v2, v2, v3
	v_mul_f32_e32 v3, v11, v11
	v_mul_f32_e32 v11, v13, v13
	v_fmac_f32_e32 v3, v10, v10
	v_fmac_f32_e32 v11, v12, v12
	v_add_f32_e32 v3, v3, v11
	v_add_f32_e32 v2, v2, v3
	v_mul_f32_e32 v3, v27, v27
	v_mul_f32_e32 v10, v9, v9
	v_fmac_f32_e32 v3, v26, v26
	v_fmac_f32_e32 v10, v8, v8
	v_add_f32_e32 v3, v3, v10
	v_add_f32_e32 v2, v2, v3
	ds_bpermute_b32 v3, v162, v2
	s_waitcnt lgkmcnt(0)
	v_add_f32_e32 v2, v2, v3
	ds_bpermute_b32 v3, v163, v2
	s_nop 0
	v_mul_f32_e32 v4, v26, v216
	v_mul_f32_e32 v5, v27, v217
	v_mul_f32_e32 v6, v8, v218
	v_mul_f32_e32 v7, v9, v219
	v_cvt_pk_bf16_f32 v38, v4, v5
	v_cvt_pk_bf16_f32 v39, v6, v7
	global_store_dwordx4 v[24:25], v[36:39], off offset:256
	s_and_saveexec_b64 s[52:53], s[4:5]
	s_cbranch_execz .LBB0_897
	s_waitcnt lgkmcnt(0)
	v_add_f32_e32 v4, v2, v3
	v_lshlrev_b64 v[2:3], 8, v[18:19]
	v_lshl_add_u64 v[2:3], s[22:23], 0, v[2:3]
	v_lshl_add_u64 v[2:3], s[50:51], 2, v[2:3]
	s_lshl_b32 s14, s66, 2
	v_lshl_add_u64 v[2:3], v[2:3], 0, s[14:15]
	global_store_dword v[2:3], v4, off

;     __device__ __forceinline__ void operator()(const f32x4 (&acc)[2][2][4][2], const Unit& u, int wr, int wc, int fr, int fq) const {
;         const int row0 = u.pm * BM + wr * 64 + fr, col0 = u.pn * BM + wc * 32 + 8 * fq;
;         f32x4 cs[2][2];
; #pragma unroll
;         for (int bj = 0; bj < 2; ++bj)
; #pragma unroll
;             for (int n = 0; n < 2; ++n) { const u32x4 c = *(const u32x4*)(cmax + col0 + bj * HALF + n * 4);
;                 cs[bj][n] = (f32x4){__uint_as_float(c.x << 16), __uint_as_float(c.y << 16), __uint_as_float(c.z << 16), __uint_as_float(c.w << 16)} * (1.0f / 127.0f); }
; #pragma unroll
;         for (int ai = 0; ai < 2; ++ai)
; #pragma unroll
;             for (int m = 0; m < 4; ++m) { const int row = row0 + ai * HALF + m * 16; const size_t ro = (size_t)row * ldc + col0; float ss = 0.f; const float rs = xs[row];
; #pragma unroll
;                 for (int bj = 0; bj < 2; ++bj)
; #pragma unroll
;                     for (int n = 0; n < 2; ++n) { const i32x4 ia = __builtin_bit_cast(i32x4, acc[ai][bj][m][n]);
;                         const f32x4 af = (f32x4){(float)ia[0], (float)ia[1], (float)ia[2], (float)ia[3]} * rs * cs[bj][n];
;                         f32x4 rv; if constexpr (RB16) { const u32x2 rb = *(const u32x2*)((const bf16_t*)R + ro + bj * HALF + n * 4); rv = (f32x4){__uint_as_float(rb.x << 16), __uint_as_float(rb.x & 0xffff0000u), __uint_as_float(rb.y << 16), __uint_as_float(rb.y & 0xffff0000u)}; }
;                         else rv = *(const f32x4*)((const float*)R + ro + bj * HALF + n * 4);
;                         const f32x4 v = af + rv; { u32x2 hb; hb.x = cvt_pk_bf16(v[0], v[1]); hb.y = cvt_pk_bf16(v[2], v[3]); *(u32x2*)(C + ro + bj * HALF + n * 4) = hb; }
;                         const f32x4 g = *(const f32x4*)(gain + col0 + bj * HALF + n * 4);
;                         u32x2 o; o.x = cvt_pk_bf16(v[0] * g[0], v[1] * g[1]); o.y = cvt_pk_bf16(v[2] * g[2], v[3] * g[3]); *(u32x2*)(HG + ro + bj * HALF + n * 4) = o;
;                         ss += (v[0] * v[0] + v[1] * v[1]) + (v[2] * v[2] + v[3] * v[3]); }
;                 ss += __shfl_xor(ss, 16); ss += __shfl_xor(ss, 32);
;                 if (fq == 0) SS[(size_t)row * 64 + u.pn * 4 + wc] = ss; }
.LBB0_1942:
	v_lshl_or_b32 v146, s10, 8, v157
	v_lshl_add_u32 v148, s48, 8, v1
	v_ashrrev_i32_e32 v147, 31, v146
	v_ashrrev_i32_e32 v149, 31, v148
	v_lshlrev_b64 v[166:167], 2, v[146:147]
	v_lshlrev_b64 v[162:163], 12, v[148:149]
	v_lshl_add_u64 v[170:171], s[24:25], 0, v[166:167]
	v_lshl_add_u64 v[162:163], v[162:163], 0, v[146:147]
	global_load_dwordx4 v[152:155], v[170:171], off
	v_lshl_add_u64 v[150:151], v[148:149], 2, s[22:23]
	v_lshlrev_b64 v[180:181], 1, v[162:163]
	global_load_dword v178, v[150:151], off
	v_lshl_add_u64 v[182:183], s[14:15], 0, v[180:181]
	global_load_dwordx2 v[174:175], v[182:183], off
	global_load_dwordx4 v[162:165], v[170:171], off offset:528
	v_cvt_f32_i32_e32 v129, v129
	v_cvt_f32_i32_e32 v128, v128
	v_cvt_f32_i32_e32 v177, v127
	v_cvt_f32_i32_e32 v176, v126
	v_lshl_add_u64 v[126:127], s[18:19], 0, v[166:167]
	global_load_dwordx4 v[166:169], v[170:171], off offset:16
	s_nop 0
	global_load_dwordx4 v[170:173], v[170:171], off offset:512
	v_cvt_f32_i32_e32 v125, v125
	v_cvt_f32_i32_e32 v124, v124
	v_cvt_f32_i32_e32 v123, v123
	v_cvt_f32_i32_e32 v122, v122
	v_lshl_add_u64 v[180:181], s[16:17], 0, v[180:181]
	v_cvt_f32_i32_e32 v121, v121
	v_cvt_f32_i32_e32 v120, v120
	v_cvt_f32_i32_e32 v119, v119
	v_cvt_f32_i32_e32 v118, v118
	v_cvt_f32_i32_e32 v117, v117
	v_cvt_f32_i32_e32 v116, v116
	v_cvt_f32_i32_e32 v115, v115
	v_cvt_f32_i32_e32 v114, v114
	s_lshl_b32 s48, s10, 2
	s_ashr_i32 s49, s48, 31
	global_load_dwordx4 v[192:195], v[126:127], off
	global_load_dwordx2 v[248:249], v[182:183], off offset:8
	global_load_dwordx4 v[196:199], v[126:127], off offset:16
	global_load_dwordx2 v[250:251], v[182:183], off offset:256
	global_load_dwordx4 v[200:203], v[126:127], off offset:512
	global_load_dwordx2 v[244:245], v[182:183], off offset:264
	global_load_dwordx4 v[204:207], v[126:127], off offset:528
	v_or_b32_e32 v190, 16, v148
	v_ashrrev_i32_e32 v191, 31, v190
	v_lshl_add_u64 v[230:231], v[190:191], 2, s[22:23]
	global_load_dword v246, v[230:231], off
	v_or_b32_e32 v252, 16, v148
	v_ashrrev_i32_e32 v253, 31, v252
	v_lshlrev_b64 v[254:255], 12, v[252:253]
	v_lshl_add_u64 v[254:255], v[254:255], 0, v[146:147]
	v_lshlrev_b64 v[254:255], 1, v[254:255]
	v_lshl_add_u64 v[190:191], s[14:15], 0, v[254:255]
	global_load_dwordx2 v[240:241], v[190:191], off
	global_load_dwordx2 v[242:243], v[190:191], off offset:8
	global_load_dwordx2 v[236:237], v[190:191], off offset:256
	global_load_dwordx2 v[238:239], v[190:191], off offset:264
	s_nop 0
	s_waitcnt vmcnt(17)
	v_lshlrev_b32_e32 v184, 16, v152
	v_lshlrev_b32_e32 v185, 16, v153
	v_lshlrev_b32_e32 v152, 16, v154
	v_lshlrev_b32_e32 v153, 16, v155
	s_waitcnt vmcnt(16)
	v_pk_mul_f32 v[154:155], v[178:179], v[176:177] op_sel_hi:[0,1]
	v_pk_mul_f32 v[176:177], v[178:179], v[128:129] op_sel_hi:[0,1]
	v_pk_mul_f32 v[152:153], v[152:153], s[36:37] op_sel_hi:[1,0]
	v_pk_mul_f32 v[128:129], v[184:185], s[36:37] op_sel_hi:[1,0]
	s_waitcnt vmcnt(15)
	v_lshlrev_b32_e32 v184, 16, v174
	v_and_b32_e32 v185, 0xffff0000, v174
	v_lshlrev_b32_e32 v174, 16, v175
	v_and_b32_e32 v175, 0xffff0000, v175
	v_pk_fma_f32 v[186:187], v[176:177], v[152:153], v[174:175]
	v_pk_fma_f32 v[154:155], v[154:155], v[128:129], v[184:185]
	s_waitcnt vmcnt(13)
	v_lshlrev_b32_e32 v166, 16, v166
	v_cvt_pk_bf16_f32 v208, v154, v155
	v_cvt_pk_bf16_f32 v209, v186, v187
	s_nop 0
	s_nop 0
	v_lshlrev_b32_e32 v167, 16, v167
	v_lshlrev_b32_e32 v168, 16, v168
	v_lshlrev_b32_e32 v169, 16, v169
	v_pk_mul_f32 v[184:185], v[178:179], v[122:123] op_sel_hi:[0,1]
	v_pk_mul_f32 v[188:189], v[178:179], v[124:125] op_sel_hi:[0,1]
	v_pk_mul_f32 v[124:125], v[168:169], s[36:37] op_sel_hi:[1,0]
	v_pk_mul_f32 v[122:123], v[166:167], s[36:37] op_sel_hi:[1,0]
	s_waitcnt vmcnt(12)
	v_lshlrev_b32_e32 v170, 16, v170
	v_lshlrev_b32_e32 v171, 16, v171
	v_lshlrev_b32_e32 v172, 16, v172
	v_lshlrev_b32_e32 v173, 16, v173
	v_lshlrev_b32_e32 v162, 16, v162
	v_lshlrev_b32_e32 v163, 16, v163
	v_lshlrev_b32_e32 v164, 16, v164
	v_lshlrev_b32_e32 v165, 16, v165
	s_nop 0
	s_waitcnt vmcnt(11)
	v_mul_f32_e32 v174, v192, v154
	v_mul_f32_e32 v175, v193, v155
	v_mul_f32_e32 v176, v194, v186
	v_mul_f32_e32 v177, v195, v187
	v_cvt_pk_bf16_f32 v212, v174, v175
	v_cvt_pk_bf16_f32 v213, v176, v177
	s_nop 0
	v_mul_f32_e32 v155, v155, v155
	s_nop 0
	v_fmac_f32_e32 v155, v154, v154
	s_nop 0
	s_waitcnt vmcnt(10)
	v_lshlrev_b32_e32 v166, 16, v248
	v_and_b32_e32 v167, 0xffff0000, v248
	v_lshlrev_b32_e32 v168, 16, v249
	v_and_b32_e32 v169, 0xffff0000, v249
	v_pk_fma_f32 v[174:175], v[188:189], v[124:125], v[168:169]
	v_pk_fma_f32 v[176:177], v[184:185], v[122:123], v[166:167]
	v_pk_mul_f32 v[184:185], v[178:179], v[118:119] op_sel_hi:[0,1]
	v_cvt_pk_bf16_f32 v210, v176, v177
	v_cvt_pk_bf16_f32 v211, v174, v175
	global_store_dwordx4 v[182:183], v[208:211], off
	s_nop 0
	v_pk_mul_f32 v[188:189], v[178:179], v[120:121] op_sel_hi:[0,1]
	v_pk_mul_f32 v[120:121], v[172:173], s[36:37] op_sel_hi:[1,0]
	v_pk_mul_f32 v[118:119], v[170:171], s[36:37] op_sel_hi:[1,0]
	s_nop 0
	s_waitcnt vmcnt(10)
	v_mul_f32_e32 v166, v196, v176
	v_mul_f32_e32 v167, v197, v177
	v_mul_f32_e32 v168, v198, v174
	v_mul_f32_e32 v169, v199, v175
	v_cvt_pk_bf16_f32 v214, v166, v167
	v_cvt_pk_bf16_f32 v215, v168, v169
	s_nop 0
	v_mul_f32_e32 v175, v175, v175
	global_store_dwordx4 v[180:181], v[212:215], off
	v_fmac_f32_e32 v175, v174, v174
	s_nop 0
	s_waitcnt vmcnt(10)
; __device__ __forceinline__ unsigned cvt_pk_bf16(float lo, float hi) { unsigned r; asm volatile("v_cvt_pk_bf16_f32 %0, %1, %2" : "=v"(r) : "v"(lo), "v"(hi)); return r; }
;     __device__ __forceinline__ void operator()(const f32x4 (&acc)[2][2][4][2], const Unit& u, int wr, int wc, int fr, int fq) const {
;     ...
;             for (int m = 0; m < 4; ++m) { const int row = row0 + ai * HALF + m * 16; const size_t ro = (size_t)row * ldc + col0; float ss = 0.f; const float rs = xs[row];
; #pragma unroll
;                 for (int bj = 0; bj < 2; ++bj)
; #pragma unroll
;                     for (int n = 0; n < 2; ++n) { const i32x4 ia = __builtin_bit_cast(i32x4, acc[ai][bj][m][n]);
;                         const f32x4 af = (f32x4){(float)ia[0], (float)ia[1], (float)ia[2], (float)ia[3]} * rs * cs[bj][n];
;                         f32x4 rv; if constexpr (RB16) { const u32x2 rb = *(const u32x2*)((const bf16_t*)R + ro + bj * HALF + n * 4); rv = (f32x4){__uint_as_float(rb.x << 16), __uint_as_float(rb.x & 0xffff0000u), __uint_as_float(rb.y << 16), __uint_as_float(rb.y & 0xffff0000u)}; }
;                         else rv = *(const f32x4*)((const float*)R + ro + bj * HALF + n * 4);
;                         const f32x4 v = af + rv; { u32x2 hb; hb.x = cvt_pk_bf16(v[0], v[1]); hb.y = cvt_pk_bf16(v[2], v[3]); *(u32x2*)(C + ro + bj * HALF + n * 4) = hb; }
;                         const f32x4 g = *(const f32x4*)(gain + col0 + bj * HALF + n * 4);
;                         u32x2 o; o.x = cvt_pk_bf16(v[0] * g[0], v[1] * g[1]); o.y = cvt_pk_bf16(v[2] * g[2], v[3] * g[3]); *(u32x2*)(HG + ro + bj * HALF + n * 4) = o;
;                         ss += (v[0] * v[0] + v[1] * v[1]) + (v[2] * v[2] + v[3] * v[3]); }
;                 ss += __shfl_xor(ss, 16); ss += __shfl_xor(ss, 32);
;                 if (fq == 0) SS[(size_t)row * 64 + u.pn * 4 + wc] = ss; }
	v_lshlrev_b32_e32 v166, 16, v250
	v_and_b32_e32 v167, 0xffff0000, v250
	v_lshlrev_b32_e32 v168, 16, v251
	v_and_b32_e32 v169, 0xffff0000, v251
	v_pk_fma_f32 v[170:171], v[188:189], v[120:121], v[168:169]
	v_pk_fma_f32 v[172:173], v[184:185], v[118:119], v[166:167]
	v_pk_mul_f32 v[184:185], v[178:179], v[114:115] op_sel_hi:[0,1]
	v_cvt_pk_bf16_f32 v208, v172, v173
	v_cvt_pk_bf16_f32 v209, v170, v171
	s_nop 0
	s_nop 0
	v_pk_mul_f32 v[178:179], v[178:179], v[116:117] op_sel_hi:[0,1]
	v_pk_mul_f32 v[116:117], v[164:165], s[36:37] op_sel_hi:[1,0]
	v_pk_mul_f32 v[114:115], v[162:163], s[36:37] op_sel_hi:[1,0]
	s_nop 0
	s_waitcnt vmcnt(9)
	v_mul_f32_e32 v166, v200, v172
	v_mul_f32_e32 v167, v201, v173
	v_mul_f32_e32 v168, v202, v170
	v_mul_f32_e32 v169, v203, v171
	v_cvt_pk_bf16_f32 v212, v166, v167
	v_cvt_pk_bf16_f32 v213, v168, v169
	s_nop 0
	v_mul_f32_e32 v171, v171, v171
	s_nop 0
	v_fmac_f32_e32 v171, v170, v170
	s_nop 0
	s_waitcnt vmcnt(8)
	v_lshlrev_b32_e32 v162, 16, v244
	v_and_b32_e32 v163, 0xffff0000, v244
	v_lshlrev_b32_e32 v164, 16, v245
	v_and_b32_e32 v165, 0xffff0000, v245
	v_pk_fma_f32 v[168:169], v[178:179], v[116:117], v[164:165]
	v_pk_fma_f32 v[178:179], v[184:185], v[114:115], v[162:163]
	v_mul_f32_e32 v170, v169, v169
	v_cvt_pk_bf16_f32 v210, v178, v179
	v_cvt_pk_bf16_f32 v211, v168, v169
	global_store_dwordx4 v[182:183], v[208:211], off offset:256
	s_nop 0
	v_mul_f32_e32 v183, v187, v187
	v_fmac_f32_e32 v183, v186, v186
	v_add_f32_e32 v154, v155, v183
	v_mul_f32_e32 v155, v177, v177
	v_fmac_f32_e32 v155, v176, v176
	v_add_f32_e32 v155, v155, v175
	v_add_f32_e32 v154, v154, v155
	v_mul_f32_e32 v155, v173, v173
	v_fmac_f32_e32 v155, v172, v172
	v_and_b32_e32 v163, 64, v161
	v_add_f32_e32 v155, v155, v171
	v_xor_b32_e32 v162, 16, v161
	v_add_u32_e32 v163, 64, v163
	v_add_f32_e32 v154, v154, v155
	v_mul_f32_e32 v155, v179, v179
	v_cmp_lt_i32_e32 vcc, v162, v163
	v_fmac_f32_e32 v155, v178, v178
	v_fmac_f32_e32 v170, v168, v168
	v_cndmask_b32_e32 v162, v161, v162, vcc
	v_add_f32_e32 v155, v155, v170
	v_lshlrev_b32_e32 v162, 2, v162
	v_add_f32_e32 v154, v154, v155
	ds_bpermute_b32 v155, v162, v154
	v_xor_b32_e32 v182, 32, v161
	v_cmp_lt_i32_e32 vcc, v182, v163
	s_waitcnt lgkmcnt(0)
	v_add_f32_e32 v154, v154, v155
	v_cndmask_b32_e32 v163, v161, v182, vcc
	v_lshlrev_b32_e32 v163, 2, v163
	ds_bpermute_b32 v155, v163, v154
	s_nop 0
	s_waitcnt vmcnt(8)
	v_mul_f32_e32 v164, v204, v178
	v_mul_f32_e32 v165, v205, v179
	v_mul_f32_e32 v166, v206, v168
	v_mul_f32_e32 v167, v207, v169
	v_cvt_pk_bf16_f32 v214, v164, v165
	v_cvt_pk_bf16_f32 v215, v166, v167
	global_store_dwordx4 v[180:181], v[212:215], off offset:256
	s_and_saveexec_b64 s[50:51], s[4:5]
	s_cbranch_execz .LBB0_1944
	s_waitcnt lgkmcnt(0)
	v_add_f32_e32 v164, v154, v155
	v_lshlrev_b64 v[154:155], 8, v[148:149]
	v_lshl_add_u64 v[154:155], s[20:21], 0, v[154:155]
	v_lshl_add_u64 v[154:155], s[48:49], 2, v[154:155]
	s_lshl_b32 s10, s64, 2
	v_lshl_add_u64 v[154:155], v[154:155], 0, s[10:11]
	global_store_dword v[154:155], v164, off
.LBB0_1944:
	s_or_b64 exec, exec, s[50:51]
	v_or_b32_e32 v230, 32, v148
	v_ashrrev_i32_e32 v231, 31, v230
	v_lshl_add_u64 v[252:253], v[230:231], 2, s[22:23]
	global_load_dword v248, v[252:253], off
	v_or_b32_e32 v254, 32, v148
	v_ashrrev_i32_e32 v255, 31, v254
	v_lshlrev_b64 v[190:191], 12, v[254:255]
	v_lshl_add_u64 v[190:191], v[190:191], 0, v[146:147]
	v_lshlrev_b64 v[190:191], 1, v[190:191]
	v_lshl_add_u64 v[230:231], s[14:15], 0, v[190:191]
	global_load_dwordx2 v[250:251], v[230:231], off
	global_load_dwordx2 v[244:245], v[230:231], off offset:8
	global_load_dwordx2 v[232:233], v[230:231], off offset:256
	global_load_dwordx2 v[234:235], v[230:231], off offset:264
	v_or_b32_e32 v154, 16, v148
	s_waitcnt lgkmcnt(0)
	v_ashrrev_i32_e32 v155, 31, v154
	v_lshlrev_b64 v[164:165], 12, v[154:155]
	v_lshl_add_u64 v[164:165], v[164:165], 0, v[146:147]
	v_lshlrev_b64 v[164:165], 1, v[164:165]
	v_lshl_add_u64 v[166:167], v[154:155], 2, s[22:23]
	v_lshl_add_u64 v[168:169], s[14:15], 0, v[164:165]
	s_nop 0
	v_cvt_f32_i32_e32 v113, v113
	s_nop 0
	v_cvt_f32_i32_e32 v111, v111
	v_cvt_f32_i32_e32 v110, v110
	v_cvt_f32_i32_e32 v112, v112
	v_cvt_f32_i32_e32 v109, v109
	v_cvt_f32_i32_e32 v107, v107
	v_cvt_f32_i32_e32 v106, v106
	v_cvt_f32_i32_e32 v108, v108
	v_lshl_add_u64 v[164:165], s[16:17], 0, v[164:165]
	v_cvt_f32_i32_e32 v105, v105
	v_cvt_f32_i32_e32 v103, v103
	v_cvt_f32_i32_e32 v102, v102
	v_cvt_f32_i32_e32 v104, v104
	v_cvt_f32_i32_e32 v101, v101
	v_cvt_f32_i32_e32 v99, v99
	v_cvt_f32_i32_e32 v98, v98
	v_cvt_f32_i32_e32 v100, v100
	s_nop 0
	s_waitcnt vmcnt(13)
	v_pk_mul_f32 v[110:111], v[246:247], v[110:111] op_sel_hi:[0,1]
	v_pk_mul_f32 v[112:113], v[246:247], v[112:113] op_sel_hi:[0,1]
	s_nop 0
	s_waitcnt vmcnt(12)
	v_lshlrev_b32_e32 v172, 16, v240
	v_and_b32_e32 v173, 0xffff0000, v240
	v_lshlrev_b32_e32 v170, 16, v241
	v_and_b32_e32 v171, 0xffff0000, v241
	v_pk_fma_f32 v[170:171], v[152:153], v[112:113], v[170:171]
	v_pk_fma_f32 v[172:173], v[128:129], v[110:111], v[172:173]
	v_pk_mul_f32 v[106:107], v[246:247], v[106:107] op_sel_hi:[0,1]
	v_cvt_pk_bf16_f32 v176, v172, v173
	v_cvt_pk_bf16_f32 v177, v170, v171
	s_nop 0
	s_nop 0
	v_pk_mul_f32 v[108:109], v[246:247], v[108:109] op_sel_hi:[0,1]
	v_pk_mul_f32 v[102:103], v[246:247], v[102:103] op_sel_hi:[0,1]
	v_pk_mul_f32 v[104:105], v[246:247], v[104:105] op_sel_hi:[0,1]
	v_pk_mul_f32 v[98:99], v[246:247], v[98:99] op_sel_hi:[0,1]
	v_pk_mul_f32 v[100:101], v[246:247], v[100:101] op_sel_hi:[0,1]
	s_nop 0
	v_mul_f32_e32 v110, v192, v172
	v_mul_f32_e32 v111, v193, v173
	v_mul_f32_e32 v112, v194, v170
	v_mul_f32_e32 v113, v195, v171
	v_cvt_pk_bf16_f32 v180, v110, v111
	v_cvt_pk_bf16_f32 v181, v112, v113
	s_nop 0
	s_nop 0
	s_nop 0
	s_nop 0
	s_waitcnt vmcnt(11)
; __device__ __forceinline__ unsigned cvt_pk_bf16(float lo, float hi) { unsigned r; asm volatile("v_cvt_pk_bf16_f32 %0, %1, %2" : "=v"(r) : "v"(lo), "v"(hi)); return r; }
;     __device__ __forceinline__ void operator()(const f32x4 (&acc)[2][2][4][2], const Unit& u, int wr, int wc, int fr, int fq) const {
;     ...
;             for (int m = 0; m < 4; ++m) { const int row = row0 + ai * HALF + m * 16; const size_t ro = (size_t)row * ldc + col0; float ss = 0.f; const float rs = xs[row];
; #pragma unroll
;                 for (int bj = 0; bj < 2; ++bj)
; #pragma unroll
;                     for (int n = 0; n < 2; ++n) { const i32x4 ia = __builtin_bit_cast(i32x4, acc[ai][bj][m][n]);
;                         const f32x4 af = (f32x4){(float)ia[0], (float)ia[1], (float)ia[2], (float)ia[3]} * rs * cs[bj][n];
;                         f32x4 rv; if constexpr (RB16) { const u32x2 rb = *(const u32x2*)((const bf16_t*)R + ro + bj * HALF + n * 4); rv = (f32x4){__uint_as_float(rb.x << 16), __uint_as_float(rb.x & 0xffff0000u), __uint_as_float(rb.y << 16), __uint_as_float(rb.y & 0xffff0000u)}; }
;                         else rv = *(const f32x4*)((const float*)R + ro + bj * HALF + n * 4);
;                         const f32x4 v = af + rv; { u32x2 hb; hb.x = cvt_pk_bf16(v[0], v[1]); hb.y = cvt_pk_bf16(v[2], v[3]); *(u32x2*)(C + ro + bj * HALF + n * 4) = hb; }
;                         const f32x4 g = *(const f32x4*)(gain + col0 + bj * HALF + n * 4);
;                         u32x2 o; o.x = cvt_pk_bf16(v[0] * g[0], v[1] * g[1]); o.y = cvt_pk_bf16(v[2] * g[2], v[3] * g[3]); *(u32x2*)(HG + ro + bj * HALF + n * 4) = o;
;                         ss += (v[0] * v[0] + v[1] * v[1]) + (v[2] * v[2] + v[3] * v[3]); }
;                 ss += __shfl_xor(ss, 16); ss += __shfl_xor(ss, 32);
;                 if (fq == 0) SS[(size_t)row * 64 + u.pn * 4 + wc] = ss; }
	v_lshlrev_b32_e32 v110, 16, v242
	v_and_b32_e32 v111, 0xffff0000, v242
	v_lshlrev_b32_e32 v112, 16, v243
	v_and_b32_e32 v113, 0xffff0000, v243
	v_pk_fma_f32 v[112:113], v[124:125], v[108:109], v[112:113]
	v_pk_fma_f32 v[110:111], v[122:123], v[106:107], v[110:111]
	s_nop 0
	v_cvt_pk_bf16_f32 v178, v110, v111
	v_cvt_pk_bf16_f32 v179, v112, v113
	global_store_dwordx4 v[168:169], v[176:179], off
	s_nop 0
	s_nop 0
	v_mul_f32_e32 v106, v196, v110
	v_mul_f32_e32 v107, v197, v111
	v_mul_f32_e32 v108, v198, v112
	v_mul_f32_e32 v109, v199, v113
	v_cvt_pk_bf16_f32 v182, v106, v107
	v_cvt_pk_bf16_f32 v183, v108, v109
	s_nop 0
	s_nop 0
	global_store_dwordx4 v[164:165], v[180:183], off
	s_nop 0
	s_waitcnt vmcnt(12)
	v_lshlrev_b32_e32 v106, 16, v236
	v_and_b32_e32 v107, 0xffff0000, v236
	v_lshlrev_b32_e32 v108, 16, v237
	v_and_b32_e32 v109, 0xffff0000, v237
	v_pk_fma_f32 v[108:109], v[120:121], v[104:105], v[108:109]
	v_pk_fma_f32 v[106:107], v[118:119], v[102:103], v[106:107]
	s_nop 0
	v_cvt_pk_bf16_f32 v176, v106, v107
	v_cvt_pk_bf16_f32 v177, v108, v109
	s_nop 0
	s_nop 0
	s_nop 0
	v_mul_f32_e32 v102, v200, v106
	v_mul_f32_e32 v103, v201, v107
	v_mul_f32_e32 v104, v202, v108
	v_mul_f32_e32 v105, v203, v109
	v_cvt_pk_bf16_f32 v180, v102, v103
	v_cvt_pk_bf16_f32 v181, v104, v105
	s_nop 0
	s_nop 0
	s_nop 0
	s_nop 0
	s_waitcnt vmcnt(11)
	v_lshlrev_b32_e32 v102, 16, v238
	v_and_b32_e32 v103, 0xffff0000, v238
	v_lshlrev_b32_e32 v104, 16, v239
	v_and_b32_e32 v105, 0xffff0000, v239
	v_pk_fma_f32 v[104:105], v[116:117], v[100:101], v[104:105]
	v_pk_fma_f32 v[166:167], v[114:115], v[98:99], v[102:103]
	s_nop 0
	v_cvt_pk_bf16_f32 v178, v166, v167
	v_cvt_pk_bf16_f32 v179, v104, v105
	global_store_dwordx4 v[168:169], v[176:179], off offset:256
	s_nop 0
	v_mul_f32_e32 v98, v173, v173
	v_mul_f32_e32 v99, v171, v171
	v_fmac_f32_e32 v98, v172, v172
	v_fmac_f32_e32 v99, v170, v170
	v_add_f32_e32 v98, v98, v99
	v_mul_f32_e32 v99, v111, v111
	v_mul_f32_e32 v111, v113, v113
	v_fmac_f32_e32 v99, v110, v110
	v_fmac_f32_e32 v111, v112, v112
	v_add_f32_e32 v99, v99, v111
	v_add_f32_e32 v98, v98, v99
	v_mul_f32_e32 v99, v107, v107
	v_mul_f32_e32 v107, v109, v109
	v_fmac_f32_e32 v99, v106, v106
	v_fmac_f32_e32 v107, v108, v108
	v_add_f32_e32 v99, v99, v107
	v_add_f32_e32 v98, v98, v99
	v_mul_f32_e32 v99, v167, v167
	v_mul_f32_e32 v106, v105, v105
	v_fmac_f32_e32 v99, v166, v166
	v_fmac_f32_e32 v106, v104, v104
	v_add_f32_e32 v99, v99, v106
	v_add_f32_e32 v98, v98, v99
	ds_bpermute_b32 v99, v162, v98
	s_waitcnt lgkmcnt(0)
	v_add_f32_e32 v98, v98, v99
	ds_bpermute_b32 v99, v163, v98
	s_nop 0
	v_mul_f32_e32 v100, v204, v166
	v_mul_f32_e32 v101, v205, v167
	v_mul_f32_e32 v102, v206, v104
	v_mul_f32_e32 v103, v207, v105
	v_cvt_pk_bf16_f32 v182, v100, v101
	v_cvt_pk_bf16_f32 v183, v102, v103
	global_store_dwordx4 v[164:165], v[180:183], off offset:256
	s_and_saveexec_b64 s[50:51], s[4:5]
	s_cbranch_execz .LBB0_1946
	s_waitcnt lgkmcnt(0)
	v_add_f32_e32 v100, v98, v99
	v_lshlrev_b64 v[98:99], 8, v[154:155]
	v_lshl_add_u64 v[98:99], s[20:21], 0, v[98:99]
	v_lshl_add_u64 v[98:99], s[48:49], 2, v[98:99]
	s_lshl_b32 s10, s64, 2
	v_lshl_add_u64 v[98:99], v[98:99], 0, s[10:11]
	global_store_dword v[98:99], v100, off
.LBB0_1946:
	s_or_b64 exec, exec, s[50:51]
	v_or_b32_e32 v252, 48, v148
	v_ashrrev_i32_e32 v253, 31, v252
	v_lshl_add_u64 v[254:255], v[252:253], 2, s[22:23]
	global_load_dword v246, v[254:255], off
	v_or_b32_e32 v190, 48, v148
	v_ashrrev_i32_e32 v191, 31, v190
	v_lshlrev_b64 v[230:231], 12, v[190:191]
	v_lshl_add_u64 v[230:231], v[230:231], 0, v[146:147]
	v_lshlrev_b64 v[230:231], 1, v[230:231]
	v_lshl_add_u64 v[252:253], s[14:15], 0, v[230:231]
	global_load_dwordx2 v[240:241], v[252:253], off
	global_load_dwordx2 v[242:243], v[252:253], off offset:8
	global_load_dwordx2 v[236:237], v[252:253], off offset:256
	global_load_dwordx2 v[238:239], v[252:253], off offset:264
	v_or_b32_e32 v98, 32, v148
	s_waitcnt lgkmcnt(0)
	v_ashrrev_i32_e32 v99, 31, v98
	v_lshlrev_b64 v[100:101], 12, v[98:99]
	v_lshl_add_u64 v[100:101], v[100:101], 0, v[146:147]
	v_lshlrev_b64 v[100:101], 1, v[100:101]
	v_lshl_add_u64 v[102:103], v[98:99], 2, s[22:23]
	v_lshl_add_u64 v[104:105], s[14:15], 0, v[100:101]
	s_nop 0
	v_cvt_f32_i32_e32 v97, v97
	s_nop 0
	v_cvt_f32_i32_e32 v95, v95
	v_cvt_f32_i32_e32 v94, v94
	v_cvt_f32_i32_e32 v96, v96
	v_cvt_f32_i32_e32 v93, v93
	v_cvt_f32_i32_e32 v91, v91
	v_cvt_f32_i32_e32 v90, v90
	v_cvt_f32_i32_e32 v92, v92
	v_lshl_add_u64 v[100:101], s[16:17], 0, v[100:101]
	v_cvt_f32_i32_e32 v89, v89
	v_cvt_f32_i32_e32 v87, v87
	v_cvt_f32_i32_e32 v86, v86
	v_cvt_f32_i32_e32 v88, v88
	v_cvt_f32_i32_e32 v85, v85
	v_cvt_f32_i32_e32 v83, v83
	v_cvt_f32_i32_e32 v82, v82
	v_cvt_f32_i32_e32 v84, v84
	s_nop 0
	s_waitcnt vmcnt(13)
	v_pk_mul_f32 v[94:95], v[248:249], v[94:95] op_sel_hi:[0,1]
	v_pk_mul_f32 v[96:97], v[248:249], v[96:97] op_sel_hi:[0,1]
	s_nop 0
	s_waitcnt vmcnt(12)
	v_lshlrev_b32_e32 v108, 16, v250
	v_and_b32_e32 v109, 0xffff0000, v250
	v_lshlrev_b32_e32 v106, 16, v251
	v_and_b32_e32 v107, 0xffff0000, v251
	v_pk_fma_f32 v[106:107], v[152:153], v[96:97], v[106:107]
	v_pk_fma_f32 v[108:109], v[128:129], v[94:95], v[108:109]
	v_pk_mul_f32 v[90:91], v[248:249], v[90:91] op_sel_hi:[0,1]
	v_cvt_pk_bf16_f32 v164, v108, v109
	v_cvt_pk_bf16_f32 v165, v106, v107
	s_nop 0
	s_nop 0
	v_pk_mul_f32 v[92:93], v[248:249], v[92:93] op_sel_hi:[0,1]
	v_pk_mul_f32 v[86:87], v[248:249], v[86:87] op_sel_hi:[0,1]
	v_pk_mul_f32 v[88:89], v[248:249], v[88:89] op_sel_hi:[0,1]
	v_pk_mul_f32 v[82:83], v[248:249], v[82:83] op_sel_hi:[0,1]
	v_pk_mul_f32 v[84:85], v[248:249], v[84:85] op_sel_hi:[0,1]
	s_nop 0
	v_mul_f32_e32 v94, v192, v108
	v_mul_f32_e32 v95, v193, v109
	v_mul_f32_e32 v96, v194, v106
	v_mul_f32_e32 v97, v195, v107
	v_cvt_pk_bf16_f32 v168, v94, v95
	v_cvt_pk_bf16_f32 v169, v96, v97
	s_nop 0
	s_nop 0
	s_nop 0
	s_nop 0
	s_waitcnt vmcnt(11)
; __device__ __forceinline__ unsigned cvt_pk_bf16(float lo, float hi) { unsigned r; asm volatile("v_cvt_pk_bf16_f32 %0, %1, %2" : "=v"(r) : "v"(lo), "v"(hi)); return r; }
;     __device__ __forceinline__ void operator()(const f32x4 (&acc)[2][2][4][2], const Unit& u, int wr, int wc, int fr, int fq) const {
;     ...
;             for (int m = 0; m < 4; ++m) { const int row = row0 + ai * HALF + m * 16; const size_t ro = (size_t)row * ldc + col0; float ss = 0.f; const float rs = xs[row];
; #pragma unroll
;                 for (int bj = 0; bj < 2; ++bj)
; #pragma unroll
;                     for (int n = 0; n < 2; ++n) { const i32x4 ia = __builtin_bit_cast(i32x4, acc[ai][bj][m][n]);
;                         const f32x4 af = (f32x4){(float)ia[0], (float)ia[1], (float)ia[2], (float)ia[3]} * rs * cs[bj][n];
;                         f32x4 rv; if constexpr (RB16) { const u32x2 rb = *(const u32x2*)((const bf16_t*)R + ro + bj * HALF + n * 4); rv = (f32x4){__uint_as_float(rb.x << 16), __uint_as_float(rb.x & 0xffff0000u), __uint_as_float(rb.y << 16), __uint_as_float(rb.y & 0xffff0000u)}; }
;                         else rv = *(const f32x4*)((const float*)R + ro + bj * HALF + n * 4);
;                         const f32x4 v = af + rv; { u32x2 hb; hb.x = cvt_pk_bf16(v[0], v[1]); hb.y = cvt_pk_bf16(v[2], v[3]); *(u32x2*)(C + ro + bj * HALF + n * 4) = hb; }
;                         const f32x4 g = *(const f32x4*)(gain + col0 + bj * HALF + n * 4);
;                         u32x2 o; o.x = cvt_pk_bf16(v[0] * g[0], v[1] * g[1]); o.y = cvt_pk_bf16(v[2] * g[2], v[3] * g[3]); *(u32x2*)(HG + ro + bj * HALF + n * 4) = o;
;                         ss += (v[0] * v[0] + v[1] * v[1]) + (v[2] * v[2] + v[3] * v[3]); }
;                 ss += __shfl_xor(ss, 16); ss += __shfl_xor(ss, 32);
;                 if (fq == 0) SS[(size_t)row * 64 + u.pn * 4 + wc] = ss; }
	v_lshlrev_b32_e32 v94, 16, v244
	v_and_b32_e32 v95, 0xffff0000, v244
	v_lshlrev_b32_e32 v96, 16, v245
	v_and_b32_e32 v97, 0xffff0000, v245
	v_pk_fma_f32 v[96:97], v[124:125], v[92:93], v[96:97]
	v_pk_fma_f32 v[94:95], v[122:123], v[90:91], v[94:95]
	s_nop 0
	v_cvt_pk_bf16_f32 v166, v94, v95
	v_cvt_pk_bf16_f32 v167, v96, v97
	global_store_dwordx4 v[104:105], v[164:167], off
	s_nop 0
	s_nop 0
	v_mul_f32_e32 v90, v196, v94
	v_mul_f32_e32 v91, v197, v95
	v_mul_f32_e32 v92, v198, v96
	v_mul_f32_e32 v93, v199, v97
	v_cvt_pk_bf16_f32 v170, v90, v91
	v_cvt_pk_bf16_f32 v171, v92, v93
	s_nop 0
	s_nop 0
	global_store_dwordx4 v[100:101], v[168:171], off
	s_nop 0
	s_waitcnt vmcnt(12)
	v_lshlrev_b32_e32 v90, 16, v232
	v_and_b32_e32 v91, 0xffff0000, v232
	v_lshlrev_b32_e32 v92, 16, v233
	v_and_b32_e32 v93, 0xffff0000, v233
	v_pk_fma_f32 v[92:93], v[120:121], v[88:89], v[92:93]
	v_pk_fma_f32 v[90:91], v[118:119], v[86:87], v[90:91]
	s_nop 0
	v_cvt_pk_bf16_f32 v164, v90, v91
	v_cvt_pk_bf16_f32 v165, v92, v93
	s_nop 0
	s_nop 0
	s_nop 0
	v_mul_f32_e32 v86, v200, v90
	v_mul_f32_e32 v87, v201, v91
	v_mul_f32_e32 v88, v202, v92
	v_mul_f32_e32 v89, v203, v93
	v_cvt_pk_bf16_f32 v168, v86, v87
	v_cvt_pk_bf16_f32 v169, v88, v89
	s_nop 0
	s_nop 0
	s_nop 0
	s_nop 0
	s_waitcnt vmcnt(11)
	v_lshlrev_b32_e32 v86, 16, v234
	v_and_b32_e32 v87, 0xffff0000, v234
	v_lshlrev_b32_e32 v88, 16, v235
	v_and_b32_e32 v89, 0xffff0000, v235
	v_pk_fma_f32 v[88:89], v[116:117], v[84:85], v[88:89]
	v_pk_fma_f32 v[102:103], v[114:115], v[82:83], v[86:87]
	s_nop 0
	v_cvt_pk_bf16_f32 v166, v102, v103
	v_cvt_pk_bf16_f32 v167, v88, v89
	global_store_dwordx4 v[104:105], v[164:167], off offset:256
	s_nop 0
	v_mul_f32_e32 v82, v109, v109
	v_mul_f32_e32 v83, v107, v107
	v_fmac_f32_e32 v82, v108, v108
	v_fmac_f32_e32 v83, v106, v106
	v_add_f32_e32 v82, v82, v83
	v_mul_f32_e32 v83, v95, v95
	v_mul_f32_e32 v95, v97, v97
	v_fmac_f32_e32 v83, v94, v94
	v_fmac_f32_e32 v95, v96, v96
	v_add_f32_e32 v83, v83, v95
	v_add_f32_e32 v82, v82, v83
	v_mul_f32_e32 v83, v91, v91
	v_mul_f32_e32 v91, v93, v93
	v_fmac_f32_e32 v83, v90, v90
	v_fmac_f32_e32 v91, v92, v92
	v_add_f32_e32 v83, v83, v91
	v_add_f32_e32 v82, v82, v83
	v_mul_f32_e32 v83, v103, v103
	v_mul_f32_e32 v90, v89, v89
	v_fmac_f32_e32 v83, v102, v102
	v_fmac_f32_e32 v90, v88, v88
	v_add_f32_e32 v83, v83, v90
	v_add_f32_e32 v82, v82, v83
	ds_bpermute_b32 v83, v162, v82
	s_waitcnt lgkmcnt(0)
	v_add_f32_e32 v82, v82, v83
	ds_bpermute_b32 v83, v163, v82
	s_nop 0
	v_mul_f32_e32 v84, v204, v102
	v_mul_f32_e32 v85, v205, v103
	v_mul_f32_e32 v86, v206, v88
	v_mul_f32_e32 v87, v207, v89
	v_cvt_pk_bf16_f32 v170, v84, v85
	v_cvt_pk_bf16_f32 v171, v86, v87
	global_store_dwordx4 v[100:101], v[168:171], off offset:256
	s_and_saveexec_b64 s[50:51], s[4:5]
	s_cbranch_execz .LBB0_1948
	s_waitcnt lgkmcnt(0)
	v_add_f32_e32 v84, v82, v83
	v_lshlrev_b64 v[82:83], 8, v[98:99]
	v_lshl_add_u64 v[82:83], s[20:21], 0, v[82:83]
	v_lshl_add_u64 v[82:83], s[48:49], 2, v[82:83]
	s_lshl_b32 s10, s64, 2
	v_lshl_add_u64 v[82:83], v[82:83], 0, s[10:11]
	global_store_dword v[82:83], v84, off
.LBB0_1948:
	s_or_b64 exec, exec, s[50:51]
	global_load_dword v248, v[150:151], off offset:512
	v_add_u32_e32 v254, 0x80, v148
	v_ashrrev_i32_e32 v255, 31, v254
	v_lshlrev_b64 v[190:191], 12, v[254:255]
	v_lshl_add_u64 v[190:191], v[190:191], 0, v[146:147]
	v_lshlrev_b64 v[190:191], 1, v[190:191]
	v_lshl_add_u64 v[230:231], s[14:15], 0, v[190:191]
	global_load_dwordx2 v[250:251], v[230:231], off
	global_load_dwordx2 v[244:245], v[230:231], off offset:8
	global_load_dwordx2 v[232:233], v[230:231], off offset:256
	global_load_dwordx2 v[234:235], v[230:231], off offset:264
	v_or_b32_e32 v82, 48, v148
	s_waitcnt lgkmcnt(0)
	v_ashrrev_i32_e32 v83, 31, v82
	v_lshlrev_b64 v[84:85], 12, v[82:83]
	v_lshl_add_u64 v[84:85], v[84:85], 0, v[146:147]
	v_lshlrev_b64 v[84:85], 1, v[84:85]
	v_lshl_add_u64 v[86:87], v[82:83], 2, s[22:23]
	v_lshl_add_u64 v[88:89], s[14:15], 0, v[84:85]
	s_nop 0
	v_cvt_f32_i32_e32 v81, v81
	s_nop 0
	v_cvt_f32_i32_e32 v79, v79
	v_cvt_f32_i32_e32 v78, v78
	v_cvt_f32_i32_e32 v80, v80
	v_cvt_f32_i32_e32 v77, v77
	v_cvt_f32_i32_e32 v75, v75
	v_cvt_f32_i32_e32 v74, v74
	v_cvt_f32_i32_e32 v76, v76
	v_lshl_add_u64 v[84:85], s[16:17], 0, v[84:85]
	v_cvt_f32_i32_e32 v73, v73
	v_cvt_f32_i32_e32 v71, v71
	v_cvt_f32_i32_e32 v70, v70
	v_cvt_f32_i32_e32 v72, v72
	v_cvt_f32_i32_e32 v69, v69
	v_cvt_f32_i32_e32 v67, v67
	v_cvt_f32_i32_e32 v66, v66
	v_cvt_f32_i32_e32 v68, v68
	s_nop 0
	s_waitcnt vmcnt(13)
	v_pk_mul_f32 v[78:79], v[246:247], v[78:79] op_sel_hi:[0,1]
	v_pk_mul_f32 v[80:81], v[246:247], v[80:81] op_sel_hi:[0,1]
	s_nop 0
	s_waitcnt vmcnt(12)
	v_lshlrev_b32_e32 v92, 16, v240
	v_and_b32_e32 v93, 0xffff0000, v240
	v_lshlrev_b32_e32 v90, 16, v241
	v_and_b32_e32 v91, 0xffff0000, v241
	v_pk_fma_f32 v[90:91], v[152:153], v[80:81], v[90:91]
	v_pk_fma_f32 v[92:93], v[128:129], v[78:79], v[92:93]
	v_pk_mul_f32 v[74:75], v[246:247], v[74:75] op_sel_hi:[0,1]
	v_cvt_pk_bf16_f32 v96, v92, v93
	v_cvt_pk_bf16_f32 v97, v90, v91
	s_nop 0
	s_nop 0
	v_pk_mul_f32 v[76:77], v[246:247], v[76:77] op_sel_hi:[0,1]
	v_pk_mul_f32 v[70:71], v[246:247], v[70:71] op_sel_hi:[0,1]
	v_pk_mul_f32 v[72:73], v[246:247], v[72:73] op_sel_hi:[0,1]
	v_pk_mul_f32 v[66:67], v[246:247], v[66:67] op_sel_hi:[0,1]
	v_pk_mul_f32 v[68:69], v[246:247], v[68:69] op_sel_hi:[0,1]
	s_nop 0
	v_mul_f32_e32 v78, v192, v92
	v_mul_f32_e32 v79, v193, v93
	v_mul_f32_e32 v80, v194, v90
	v_mul_f32_e32 v81, v195, v91
	v_cvt_pk_bf16_f32 v100, v78, v79
	v_cvt_pk_bf16_f32 v101, v80, v81
	s_nop 0
	s_nop 0
	s_nop 0
	s_nop 0
	s_waitcnt vmcnt(11)
; __device__ __forceinline__ unsigned cvt_pk_bf16(float lo, float hi) { unsigned r; asm volatile("v_cvt_pk_bf16_f32 %0, %1, %2" : "=v"(r) : "v"(lo), "v"(hi)); return r; }
;     __device__ __forceinline__ void operator()(const f32x4 (&acc)[2][2][4][2], const Unit& u, int wr, int wc, int fr, int fq) const {
;     ...
;             for (int m = 0; m < 4; ++m) { const int row = row0 + ai * HALF + m * 16; const size_t ro = (size_t)row * ldc + col0; float ss = 0.f; const float rs = xs[row];
; #pragma unroll
;                 for (int bj = 0; bj < 2; ++bj)
; #pragma unroll
;                     for (int n = 0; n < 2; ++n) { const i32x4 ia = __builtin_bit_cast(i32x4, acc[ai][bj][m][n]);
;                         const f32x4 af = (f32x4){(float)ia[0], (float)ia[1], (float)ia[2], (float)ia[3]} * rs * cs[bj][n];
;                         f32x4 rv; if constexpr (RB16) { const u32x2 rb = *(const u32x2*)((const bf16_t*)R + ro + bj * HALF + n * 4); rv = (f32x4){__uint_as_float(rb.x << 16), __uint_as_float(rb.x & 0xffff0000u), __uint_as_float(rb.y << 16), __uint_as_float(rb.y & 0xffff0000u)}; }
;                         else rv = *(const f32x4*)((const float*)R + ro + bj * HALF + n * 4);
;                         const f32x4 v = af + rv; { u32x2 hb; hb.x = cvt_pk_bf16(v[0], v[1]); hb.y = cvt_pk_bf16(v[2], v[3]); *(u32x2*)(C + ro + bj * HALF + n * 4) = hb; }
;                         const f32x4 g = *(const f32x4*)(gain + col0 + bj * HALF + n * 4);
;                         u32x2 o; o.x = cvt_pk_bf16(v[0] * g[0], v[1] * g[1]); o.y = cvt_pk_bf16(v[2] * g[2], v[3] * g[3]); *(u32x2*)(HG + ro + bj * HALF + n * 4) = o;
;                         ss += (v[0] * v[0] + v[1] * v[1]) + (v[2] * v[2] + v[3] * v[3]); }
;                 ss += __shfl_xor(ss, 16); ss += __shfl_xor(ss, 32);
;                 if (fq == 0) SS[(size_t)row * 64 + u.pn * 4 + wc] = ss; }
	v_lshlrev_b32_e32 v78, 16, v242
	v_and_b32_e32 v79, 0xffff0000, v242
	v_lshlrev_b32_e32 v80, 16, v243
	v_and_b32_e32 v81, 0xffff0000, v243
	v_pk_fma_f32 v[80:81], v[124:125], v[76:77], v[80:81]
	v_pk_fma_f32 v[78:79], v[122:123], v[74:75], v[78:79]
	s_nop 0
	v_cvt_pk_bf16_f32 v98, v78, v79
	v_cvt_pk_bf16_f32 v99, v80, v81
	global_store_dwordx4 v[88:89], v[96:99], off
	s_nop 0
	s_nop 0
	v_mul_f32_e32 v74, v196, v78
	v_mul_f32_e32 v75, v197, v79
	v_mul_f32_e32 v76, v198, v80
	v_mul_f32_e32 v77, v199, v81
	v_cvt_pk_bf16_f32 v102, v74, v75
	v_cvt_pk_bf16_f32 v103, v76, v77
	s_nop 0
	s_nop 0
	global_store_dwordx4 v[84:85], v[100:103], off
	s_nop 0
	s_waitcnt vmcnt(12)
	v_lshlrev_b32_e32 v74, 16, v236
	v_and_b32_e32 v75, 0xffff0000, v236
	v_lshlrev_b32_e32 v76, 16, v237
	v_and_b32_e32 v77, 0xffff0000, v237
	v_pk_fma_f32 v[76:77], v[120:121], v[72:73], v[76:77]
	v_pk_fma_f32 v[74:75], v[118:119], v[70:71], v[74:75]
	s_nop 0
	v_cvt_pk_bf16_f32 v96, v74, v75
	v_cvt_pk_bf16_f32 v97, v76, v77
	s_nop 0
	s_nop 0
	s_nop 0
	v_mul_f32_e32 v70, v200, v74
	v_mul_f32_e32 v71, v201, v75
	v_mul_f32_e32 v72, v202, v76
	v_mul_f32_e32 v73, v203, v77
	v_cvt_pk_bf16_f32 v100, v70, v71
	v_cvt_pk_bf16_f32 v101, v72, v73
	s_nop 0
	s_nop 0
	s_nop 0
	s_nop 0
	s_waitcnt vmcnt(11)
	v_lshlrev_b32_e32 v70, 16, v238
	v_and_b32_e32 v71, 0xffff0000, v238
	v_lshlrev_b32_e32 v72, 16, v239
	v_and_b32_e32 v73, 0xffff0000, v239
	v_pk_fma_f32 v[72:73], v[116:117], v[68:69], v[72:73]
	v_pk_fma_f32 v[86:87], v[114:115], v[66:67], v[70:71]
	s_nop 0
	v_cvt_pk_bf16_f32 v98, v86, v87
	v_cvt_pk_bf16_f32 v99, v72, v73
	global_store_dwordx4 v[88:89], v[96:99], off offset:256
	s_nop 0
	v_mul_f32_e32 v66, v93, v93
	v_mul_f32_e32 v67, v91, v91
	v_fmac_f32_e32 v66, v92, v92
	v_fmac_f32_e32 v67, v90, v90
	v_add_f32_e32 v66, v66, v67
	v_mul_f32_e32 v67, v79, v79
	v_mul_f32_e32 v79, v81, v81
	v_fmac_f32_e32 v67, v78, v78
	v_fmac_f32_e32 v79, v80, v80
	v_add_f32_e32 v67, v67, v79
	v_add_f32_e32 v66, v66, v67
	v_mul_f32_e32 v67, v75, v75
	v_mul_f32_e32 v75, v77, v77
	v_fmac_f32_e32 v67, v74, v74
	v_fmac_f32_e32 v75, v76, v76
	v_add_f32_e32 v67, v67, v75
	v_add_f32_e32 v66, v66, v67
	v_mul_f32_e32 v67, v87, v87
	v_mul_f32_e32 v74, v73, v73
	v_fmac_f32_e32 v67, v86, v86
	v_fmac_f32_e32 v74, v72, v72
	v_add_f32_e32 v67, v67, v74
	v_add_f32_e32 v66, v66, v67
	ds_bpermute_b32 v67, v162, v66
	s_waitcnt lgkmcnt(0)
	v_add_f32_e32 v66, v66, v67
	ds_bpermute_b32 v67, v163, v66
	s_nop 0
	v_mul_f32_e32 v68, v204, v86
	v_mul_f32_e32 v69, v205, v87
	v_mul_f32_e32 v70, v206, v72
	v_mul_f32_e32 v71, v207, v73
	v_cvt_pk_bf16_f32 v102, v68, v69
	v_cvt_pk_bf16_f32 v103, v70, v71
	global_store_dwordx4 v[84:85], v[100:103], off offset:256
	s_and_saveexec_b64 s[50:51], s[4:5]
	s_cbranch_execz .LBB0_1950
	s_waitcnt lgkmcnt(0)
	v_add_f32_e32 v68, v66, v67
	v_lshlrev_b64 v[66:67], 8, v[82:83]
	v_lshl_add_u64 v[66:67], s[20:21], 0, v[66:67]
	v_lshl_add_u64 v[66:67], s[48:49], 2, v[66:67]
	s_lshl_b32 s10, s64, 2
	v_lshl_add_u64 v[66:67], v[66:67], 0, s[10:11]
	global_store_dword v[66:67], v68, off
.LBB0_1950:
	s_or_b64 exec, exec, s[50:51]
	global_load_dword v246, v[150:151], off offset:576
	v_add_u32_e32 v252, 0x90, v148
	v_ashrrev_i32_e32 v253, 31, v252
	v_lshlrev_b64 v[254:255], 12, v[252:253]
	v_lshl_add_u64 v[254:255], v[254:255], 0, v[146:147]
	v_lshlrev_b64 v[254:255], 1, v[254:255]
	v_lshl_add_u64 v[190:191], s[14:15], 0, v[254:255]
	global_load_dwordx2 v[240:241], v[190:191], off
	global_load_dwordx2 v[242:243], v[190:191], off offset:8
	global_load_dwordx2 v[236:237], v[190:191], off offset:256
	global_load_dwordx2 v[238:239], v[190:191], off offset:264
	v_add_u32_e32 v66, 0x80, v148
	s_waitcnt lgkmcnt(0)
	v_ashrrev_i32_e32 v67, 31, v66
	v_lshlrev_b64 v[68:69], 12, v[66:67]
	v_lshl_add_u64 v[68:69], v[68:69], 0, v[146:147]
	v_lshlrev_b64 v[68:69], 1, v[68:69]
	v_lshl_add_u64 v[72:73], s[14:15], 0, v[68:69]
	s_nop 0
	s_nop 0
	v_cvt_f32_i32_e32 v65, v65
	v_cvt_f32_i32_e32 v63, v63
	v_cvt_f32_i32_e32 v62, v62
	v_cvt_f32_i32_e32 v64, v64
	v_cvt_f32_i32_e32 v61, v61
	v_cvt_f32_i32_e32 v59, v59
	v_cvt_f32_i32_e32 v58, v58
	v_cvt_f32_i32_e32 v60, v60
	v_lshl_add_u64 v[68:69], s[16:17], 0, v[68:69]
	v_cvt_f32_i32_e32 v57, v57
	v_cvt_f32_i32_e32 v55, v55
	v_cvt_f32_i32_e32 v54, v54
	v_cvt_f32_i32_e32 v56, v56
	v_cvt_f32_i32_e32 v53, v53
	v_cvt_f32_i32_e32 v51, v51
	v_cvt_f32_i32_e32 v50, v50
	v_cvt_f32_i32_e32 v52, v52
	s_nop 0
	s_waitcnt vmcnt(13)
	v_pk_mul_f32 v[62:63], v[248:249], v[62:63] op_sel_hi:[0,1]
	v_pk_mul_f32 v[64:65], v[248:249], v[64:65] op_sel_hi:[0,1]
	s_nop 0
	s_waitcnt vmcnt(12)
	v_lshlrev_b32_e32 v76, 16, v250
	v_and_b32_e32 v77, 0xffff0000, v250
	v_lshlrev_b32_e32 v74, 16, v251
	v_and_b32_e32 v75, 0xffff0000, v251
	v_pk_fma_f32 v[74:75], v[152:153], v[64:65], v[74:75]
	v_pk_fma_f32 v[76:77], v[128:129], v[62:63], v[76:77]
	v_pk_mul_f32 v[58:59], v[248:249], v[58:59] op_sel_hi:[0,1]
	v_cvt_pk_bf16_f32 v80, v76, v77
	v_cvt_pk_bf16_f32 v81, v74, v75
	s_nop 0
	s_nop 0
	v_pk_mul_f32 v[60:61], v[248:249], v[60:61] op_sel_hi:[0,1]
	v_pk_mul_f32 v[54:55], v[248:249], v[54:55] op_sel_hi:[0,1]
	v_pk_mul_f32 v[56:57], v[248:249], v[56:57] op_sel_hi:[0,1]
	v_pk_mul_f32 v[50:51], v[248:249], v[50:51] op_sel_hi:[0,1]
	v_pk_mul_f32 v[52:53], v[248:249], v[52:53] op_sel_hi:[0,1]
	s_nop 0
	v_mul_f32_e32 v62, v192, v76
	v_mul_f32_e32 v63, v193, v77
	v_mul_f32_e32 v64, v194, v74
	v_mul_f32_e32 v65, v195, v75
	v_cvt_pk_bf16_f32 v84, v62, v63
	v_cvt_pk_bf16_f32 v85, v64, v65
	s_nop 0
	s_nop 0
	s_nop 0
	s_nop 0
	s_waitcnt vmcnt(11)
; __device__ __forceinline__ unsigned cvt_pk_bf16(float lo, float hi) { unsigned r; asm volatile("v_cvt_pk_bf16_f32 %0, %1, %2" : "=v"(r) : "v"(lo), "v"(hi)); return r; }
;     __device__ __forceinline__ void operator()(const f32x4 (&acc)[2][2][4][2], const Unit& u, int wr, int wc, int fr, int fq) const {
;     ...
;             for (int m = 0; m < 4; ++m) { const int row = row0 + ai * HALF + m * 16; const size_t ro = (size_t)row * ldc + col0; float ss = 0.f; const float rs = xs[row];
; #pragma unroll
;                 for (int bj = 0; bj < 2; ++bj)
; #pragma unroll
;                     for (int n = 0; n < 2; ++n) { const i32x4 ia = __builtin_bit_cast(i32x4, acc[ai][bj][m][n]);
;                         const f32x4 af = (f32x4){(float)ia[0], (float)ia[1], (float)ia[2], (float)ia[3]} * rs * cs[bj][n];
;                         f32x4 rv; if constexpr (RB16) { const u32x2 rb = *(const u32x2*)((const bf16_t*)R + ro + bj * HALF + n * 4); rv = (f32x4){__uint_as_float(rb.x << 16), __uint_as_float(rb.x & 0xffff0000u), __uint_as_float(rb.y << 16), __uint_as_float(rb.y & 0xffff0000u)}; }
;                         else rv = *(const f32x4*)((const float*)R + ro + bj * HALF + n * 4);
;                         const f32x4 v = af + rv; { u32x2 hb; hb.x = cvt_pk_bf16(v[0], v[1]); hb.y = cvt_pk_bf16(v[2], v[3]); *(u32x2*)(C + ro + bj * HALF + n * 4) = hb; }
;                         const f32x4 g = *(const f32x4*)(gain + col0 + bj * HALF + n * 4);
;                         u32x2 o; o.x = cvt_pk_bf16(v[0] * g[0], v[1] * g[1]); o.y = cvt_pk_bf16(v[2] * g[2], v[3] * g[3]); *(u32x2*)(HG + ro + bj * HALF + n * 4) = o;
;                         ss += (v[0] * v[0] + v[1] * v[1]) + (v[2] * v[2] + v[3] * v[3]); }
;                 ss += __shfl_xor(ss, 16); ss += __shfl_xor(ss, 32);
;                 if (fq == 0) SS[(size_t)row * 64 + u.pn * 4 + wc] = ss; }
	v_lshlrev_b32_e32 v62, 16, v244
	v_and_b32_e32 v63, 0xffff0000, v244
	v_lshlrev_b32_e32 v64, 16, v245
	v_and_b32_e32 v65, 0xffff0000, v245
	v_pk_fma_f32 v[64:65], v[124:125], v[60:61], v[64:65]
	v_pk_fma_f32 v[62:63], v[122:123], v[58:59], v[62:63]
	s_nop 0
	v_cvt_pk_bf16_f32 v82, v62, v63
	v_cvt_pk_bf16_f32 v83, v64, v65
	global_store_dwordx4 v[72:73], v[80:83], off
	s_nop 0
	s_nop 0
	v_mul_f32_e32 v58, v196, v62
	v_mul_f32_e32 v59, v197, v63
	v_mul_f32_e32 v60, v198, v64
	v_mul_f32_e32 v61, v199, v65
	v_cvt_pk_bf16_f32 v86, v58, v59
	v_cvt_pk_bf16_f32 v87, v60, v61
	s_nop 0
	s_nop 0
	global_store_dwordx4 v[68:69], v[84:87], off
	s_nop 0
	s_waitcnt vmcnt(12)
	v_lshlrev_b32_e32 v58, 16, v232
	v_and_b32_e32 v59, 0xffff0000, v232
	v_lshlrev_b32_e32 v60, 16, v233
	v_and_b32_e32 v61, 0xffff0000, v233
	v_pk_fma_f32 v[60:61], v[120:121], v[56:57], v[60:61]
	v_pk_fma_f32 v[58:59], v[118:119], v[54:55], v[58:59]
	s_nop 0
	v_cvt_pk_bf16_f32 v80, v58, v59
	v_cvt_pk_bf16_f32 v81, v60, v61
	s_nop 0
	s_nop 0
	s_nop 0
	v_mul_f32_e32 v54, v200, v58
	v_mul_f32_e32 v55, v201, v59
	v_mul_f32_e32 v56, v202, v60
	v_mul_f32_e32 v57, v203, v61
	v_cvt_pk_bf16_f32 v84, v54, v55
	v_cvt_pk_bf16_f32 v85, v56, v57
	s_nop 0
	s_nop 0
	s_nop 0
	s_nop 0
	s_waitcnt vmcnt(11)
	v_lshlrev_b32_e32 v54, 16, v234
	v_and_b32_e32 v55, 0xffff0000, v234
	v_lshlrev_b32_e32 v56, 16, v235
	v_and_b32_e32 v57, 0xffff0000, v235
	v_pk_fma_f32 v[56:57], v[116:117], v[52:53], v[56:57]
	v_pk_fma_f32 v[70:71], v[114:115], v[50:51], v[54:55]
	s_nop 0
	v_cvt_pk_bf16_f32 v82, v70, v71
	v_cvt_pk_bf16_f32 v83, v56, v57
	global_store_dwordx4 v[72:73], v[80:83], off offset:256
	s_nop 0
	v_mul_f32_e32 v50, v77, v77
	v_mul_f32_e32 v51, v75, v75
	v_fmac_f32_e32 v50, v76, v76
	v_fmac_f32_e32 v51, v74, v74
	v_add_f32_e32 v50, v50, v51
	v_mul_f32_e32 v51, v63, v63
	v_mul_f32_e32 v63, v65, v65
	v_fmac_f32_e32 v51, v62, v62
	v_fmac_f32_e32 v63, v64, v64
	v_add_f32_e32 v51, v51, v63
	v_add_f32_e32 v50, v50, v51
	v_mul_f32_e32 v51, v59, v59
	v_mul_f32_e32 v59, v61, v61
	v_fmac_f32_e32 v51, v58, v58
	v_fmac_f32_e32 v59, v60, v60
	v_add_f32_e32 v51, v51, v59
	v_add_f32_e32 v50, v50, v51
	v_mul_f32_e32 v51, v71, v71
	v_mul_f32_e32 v58, v57, v57
	v_fmac_f32_e32 v51, v70, v70
	v_fmac_f32_e32 v58, v56, v56
	v_add_f32_e32 v51, v51, v58
	v_add_f32_e32 v50, v50, v51
	ds_bpermute_b32 v51, v162, v50
	s_waitcnt lgkmcnt(0)
	v_add_f32_e32 v50, v50, v51
	ds_bpermute_b32 v51, v163, v50
	s_nop 0
	v_mul_f32_e32 v52, v204, v70
	v_mul_f32_e32 v53, v205, v71
	v_mul_f32_e32 v54, v206, v56
	v_mul_f32_e32 v55, v207, v57
	v_cvt_pk_bf16_f32 v86, v52, v53
	v_cvt_pk_bf16_f32 v87, v54, v55
	global_store_dwordx4 v[68:69], v[84:87], off offset:256
	s_and_saveexec_b64 s[50:51], s[4:5]
	s_cbranch_execz .LBB0_1952
	s_waitcnt lgkmcnt(0)
	v_add_f32_e32 v52, v50, v51
	v_lshlrev_b64 v[50:51], 8, v[66:67]
	v_lshl_add_u64 v[50:51], s[20:21], 0, v[50:51]
	v_lshl_add_u64 v[50:51], s[48:49], 2, v[50:51]
	s_lshl_b32 s10, s64, 2
	v_lshl_add_u64 v[50:51], v[50:51], 0, s[10:11]
	global_store_dword v[50:51], v52, off
.LBB0_1952:
	s_or_b64 exec, exec, s[50:51]
	global_load_dword v248, v[150:151], off offset:640
	v_add_u32_e32 v230, 0xa0, v148
	v_ashrrev_i32_e32 v231, 31, v230
	v_lshlrev_b64 v[252:253], 12, v[230:231]
	v_lshl_add_u64 v[252:253], v[252:253], 0, v[146:147]
	v_lshlrev_b64 v[252:253], 1, v[252:253]
	v_lshl_add_u64 v[254:255], s[14:15], 0, v[252:253]
	global_load_dwordx2 v[250:251], v[254:255], off
	global_load_dwordx2 v[244:245], v[254:255], off offset:8
	global_load_dwordx2 v[232:233], v[254:255], off offset:256
	global_load_dwordx2 v[234:235], v[254:255], off offset:264
	v_add_u32_e32 v50, 0x90, v148
	s_waitcnt lgkmcnt(0)
	v_ashrrev_i32_e32 v51, 31, v50
	v_lshlrev_b64 v[52:53], 12, v[50:51]
	v_lshl_add_u64 v[52:53], v[52:53], 0, v[146:147]
	v_lshlrev_b64 v[52:53], 1, v[52:53]
	v_lshl_add_u64 v[56:57], s[14:15], 0, v[52:53]
	s_nop 0
	s_nop 0
	v_cvt_f32_i32_e32 v49, v49
	v_cvt_f32_i32_e32 v47, v47
	v_cvt_f32_i32_e32 v46, v46
	v_cvt_f32_i32_e32 v48, v48
	v_cvt_f32_i32_e32 v45, v45
	v_cvt_f32_i32_e32 v43, v43
	v_cvt_f32_i32_e32 v42, v42
	v_cvt_f32_i32_e32 v44, v44
	v_lshl_add_u64 v[52:53], s[16:17], 0, v[52:53]
	v_cvt_f32_i32_e32 v41, v41
	v_cvt_f32_i32_e32 v39, v39
	v_cvt_f32_i32_e32 v38, v38
	v_cvt_f32_i32_e32 v40, v40
	v_cvt_f32_i32_e32 v37, v37
	v_cvt_f32_i32_e32 v35, v35
	v_cvt_f32_i32_e32 v34, v34
	v_cvt_f32_i32_e32 v36, v36
	s_nop 0
	s_waitcnt vmcnt(13)
	v_pk_mul_f32 v[46:47], v[246:247], v[46:47] op_sel_hi:[0,1]
	v_pk_mul_f32 v[48:49], v[246:247], v[48:49] op_sel_hi:[0,1]
	s_nop 0
	s_waitcnt vmcnt(12)
	v_lshlrev_b32_e32 v60, 16, v240
	v_and_b32_e32 v61, 0xffff0000, v240
	v_lshlrev_b32_e32 v58, 16, v241
	v_and_b32_e32 v59, 0xffff0000, v241
	v_pk_fma_f32 v[58:59], v[152:153], v[48:49], v[58:59]
	v_pk_fma_f32 v[60:61], v[128:129], v[46:47], v[60:61]
	v_pk_mul_f32 v[42:43], v[246:247], v[42:43] op_sel_hi:[0,1]
	v_cvt_pk_bf16_f32 v64, v60, v61
	v_cvt_pk_bf16_f32 v65, v58, v59
	s_nop 0
	s_nop 0
	v_pk_mul_f32 v[44:45], v[246:247], v[44:45] op_sel_hi:[0,1]
	v_pk_mul_f32 v[38:39], v[246:247], v[38:39] op_sel_hi:[0,1]
	v_pk_mul_f32 v[40:41], v[246:247], v[40:41] op_sel_hi:[0,1]
	v_pk_mul_f32 v[34:35], v[246:247], v[34:35] op_sel_hi:[0,1]
	v_pk_mul_f32 v[36:37], v[246:247], v[36:37] op_sel_hi:[0,1]
	s_nop 0
	v_mul_f32_e32 v46, v192, v60
	v_mul_f32_e32 v47, v193, v61
	v_mul_f32_e32 v48, v194, v58
	v_mul_f32_e32 v49, v195, v59
	v_cvt_pk_bf16_f32 v68, v46, v47
	v_cvt_pk_bf16_f32 v69, v48, v49
	s_nop 0
	s_nop 0
	s_nop 0
	s_nop 0
	s_waitcnt vmcnt(11)
; __device__ __forceinline__ unsigned cvt_pk_bf16(float lo, float hi) { unsigned r; asm volatile("v_cvt_pk_bf16_f32 %0, %1, %2" : "=v"(r) : "v"(lo), "v"(hi)); return r; }
;     __device__ __forceinline__ void operator()(const f32x4 (&acc)[2][2][4][2], const Unit& u, int wr, int wc, int fr, int fq) const {
;     ...
;             for (int m = 0; m < 4; ++m) { const int row = row0 + ai * HALF + m * 16; const size_t ro = (size_t)row * ldc + col0; float ss = 0.f; const float rs = xs[row];
; #pragma unroll
;                 for (int bj = 0; bj < 2; ++bj)
; #pragma unroll
;                     for (int n = 0; n < 2; ++n) { const i32x4 ia = __builtin_bit_cast(i32x4, acc[ai][bj][m][n]);
;                         const f32x4 af = (f32x4){(float)ia[0], (float)ia[1], (float)ia[2], (float)ia[3]} * rs * cs[bj][n];
;                         f32x4 rv; if constexpr (RB16) { const u32x2 rb = *(const u32x2*)((const bf16_t*)R + ro + bj * HALF + n * 4); rv = (f32x4){__uint_as_float(rb.x << 16), __uint_as_float(rb.x & 0xffff0000u), __uint_as_float(rb.y << 16), __uint_as_float(rb.y & 0xffff0000u)}; }
;                         else rv = *(const f32x4*)((const float*)R + ro + bj * HALF + n * 4);
;                         const f32x4 v = af + rv; { u32x2 hb; hb.x = cvt_pk_bf16(v[0], v[1]); hb.y = cvt_pk_bf16(v[2], v[3]); *(u32x2*)(C + ro + bj * HALF + n * 4) = hb; }
;                         const f32x4 g = *(const f32x4*)(gain + col0 + bj * HALF + n * 4);
;                         u32x2 o; o.x = cvt_pk_bf16(v[0] * g[0], v[1] * g[1]); o.y = cvt_pk_bf16(v[2] * g[2], v[3] * g[3]); *(u32x2*)(HG + ro + bj * HALF + n * 4) = o;
;                         ss += (v[0] * v[0] + v[1] * v[1]) + (v[2] * v[2] + v[3] * v[3]); }
;                 ss += __shfl_xor(ss, 16); ss += __shfl_xor(ss, 32);
;                 if (fq == 0) SS[(size_t)row * 64 + u.pn * 4 + wc] = ss; }
	v_lshlrev_b32_e32 v46, 16, v242
	v_and_b32_e32 v47, 0xffff0000, v242
	v_lshlrev_b32_e32 v48, 16, v243
	v_and_b32_e32 v49, 0xffff0000, v243
	v_pk_fma_f32 v[48:49], v[124:125], v[44:45], v[48:49]
	v_pk_fma_f32 v[46:47], v[122:123], v[42:43], v[46:47]
	s_nop 0
	v_cvt_pk_bf16_f32 v66, v46, v47
	v_cvt_pk_bf16_f32 v67, v48, v49
	global_store_dwordx4 v[56:57], v[64:67], off
	s_nop 0
	s_nop 0
	v_mul_f32_e32 v42, v196, v46
	v_mul_f32_e32 v43, v197, v47
	v_mul_f32_e32 v44, v198, v48
	v_mul_f32_e32 v45, v199, v49
	v_cvt_pk_bf16_f32 v70, v42, v43
	v_cvt_pk_bf16_f32 v71, v44, v45
	s_nop 0
	s_nop 0
	global_store_dwordx4 v[52:53], v[68:71], off
	s_nop 0
	s_waitcnt vmcnt(12)
	v_lshlrev_b32_e32 v42, 16, v236
	v_and_b32_e32 v43, 0xffff0000, v236
	v_lshlrev_b32_e32 v44, 16, v237
	v_and_b32_e32 v45, 0xffff0000, v237
	v_pk_fma_f32 v[44:45], v[120:121], v[40:41], v[44:45]
	v_pk_fma_f32 v[42:43], v[118:119], v[38:39], v[42:43]
	s_nop 0
	v_cvt_pk_bf16_f32 v64, v42, v43
	v_cvt_pk_bf16_f32 v65, v44, v45
	s_nop 0
	s_nop 0
	s_nop 0
	v_mul_f32_e32 v38, v200, v42
	v_mul_f32_e32 v39, v201, v43
	v_mul_f32_e32 v40, v202, v44
	v_mul_f32_e32 v41, v203, v45
	v_cvt_pk_bf16_f32 v68, v38, v39
	v_cvt_pk_bf16_f32 v69, v40, v41
	s_nop 0
	s_nop 0
	s_nop 0
	s_nop 0
	s_waitcnt vmcnt(11)
	v_lshlrev_b32_e32 v38, 16, v238
	v_and_b32_e32 v39, 0xffff0000, v238
	v_lshlrev_b32_e32 v40, 16, v239
	v_and_b32_e32 v41, 0xffff0000, v239
	v_pk_fma_f32 v[40:41], v[116:117], v[36:37], v[40:41]
	v_pk_fma_f32 v[54:55], v[114:115], v[34:35], v[38:39]
	s_nop 0
	v_cvt_pk_bf16_f32 v66, v54, v55
	v_cvt_pk_bf16_f32 v67, v40, v41
	global_store_dwordx4 v[56:57], v[64:67], off offset:256
	s_nop 0
	v_mul_f32_e32 v34, v61, v61
	v_mul_f32_e32 v35, v59, v59
	v_fmac_f32_e32 v34, v60, v60
	v_fmac_f32_e32 v35, v58, v58
	v_add_f32_e32 v34, v34, v35
	v_mul_f32_e32 v35, v47, v47
	v_mul_f32_e32 v47, v49, v49
	v_fmac_f32_e32 v35, v46, v46
	v_fmac_f32_e32 v47, v48, v48
	v_add_f32_e32 v35, v35, v47
	v_add_f32_e32 v34, v34, v35
	v_mul_f32_e32 v35, v43, v43
	v_mul_f32_e32 v43, v45, v45
	v_fmac_f32_e32 v35, v42, v42
	v_fmac_f32_e32 v43, v44, v44
	v_add_f32_e32 v35, v35, v43
	v_add_f32_e32 v34, v34, v35
	v_mul_f32_e32 v35, v55, v55
	v_mul_f32_e32 v42, v41, v41
	v_fmac_f32_e32 v35, v54, v54
	v_fmac_f32_e32 v42, v40, v40
	v_add_f32_e32 v35, v35, v42
	v_add_f32_e32 v34, v34, v35
	ds_bpermute_b32 v35, v162, v34
	s_waitcnt lgkmcnt(0)
	v_add_f32_e32 v34, v34, v35
	ds_bpermute_b32 v35, v163, v34
	s_nop 0
	v_mul_f32_e32 v36, v204, v54
	v_mul_f32_e32 v37, v205, v55
	v_mul_f32_e32 v38, v206, v40
	v_mul_f32_e32 v39, v207, v41
	v_cvt_pk_bf16_f32 v70, v36, v37
	v_cvt_pk_bf16_f32 v71, v38, v39
	global_store_dwordx4 v[52:53], v[68:71], off offset:256
	s_and_saveexec_b64 s[50:51], s[4:5]
	s_cbranch_execz .LBB0_1954
	s_waitcnt lgkmcnt(0)
	v_add_f32_e32 v36, v34, v35
	v_lshlrev_b64 v[34:35], 8, v[50:51]
	v_lshl_add_u64 v[34:35], s[20:21], 0, v[34:35]
	v_lshl_add_u64 v[34:35], s[48:49], 2, v[34:35]
	s_lshl_b32 s10, s64, 2
	v_lshl_add_u64 v[34:35], v[34:35], 0, s[10:11]
	global_store_dword v[34:35], v36, off
.LBB0_1954:
	s_or_b64 exec, exec, s[50:51]
	global_load_dword v246, v[150:151], off offset:704
	v_add_u32_e32 v190, 0xb0, v148
	v_ashrrev_i32_e32 v191, 31, v190
	v_lshlrev_b64 v[230:231], 12, v[190:191]
	v_lshl_add_u64 v[230:231], v[230:231], 0, v[146:147]
	v_lshlrev_b64 v[230:231], 1, v[230:231]
	v_lshl_add_u64 v[252:253], s[14:15], 0, v[230:231]
	global_load_dwordx2 v[240:241], v[252:253], off
	global_load_dwordx2 v[242:243], v[252:253], off offset:8
	global_load_dwordx2 v[236:237], v[252:253], off offset:256
	global_load_dwordx2 v[238:239], v[252:253], off offset:264
	v_add_u32_e32 v34, 0xa0, v148
	s_waitcnt lgkmcnt(0)
	v_ashrrev_i32_e32 v35, 31, v34
	v_lshlrev_b64 v[36:37], 12, v[34:35]
	v_lshl_add_u64 v[36:37], v[36:37], 0, v[146:147]
	v_lshlrev_b64 v[36:37], 1, v[36:37]
	v_lshl_add_u64 v[40:41], s[14:15], 0, v[36:37]
	s_nop 0
	s_nop 0
	v_cvt_f32_i32_e32 v33, v33
	v_cvt_f32_i32_e32 v31, v31
	v_cvt_f32_i32_e32 v30, v30
	v_cvt_f32_i32_e32 v32, v32
	v_cvt_f32_i32_e32 v29, v29
	v_cvt_f32_i32_e32 v27, v27
	v_cvt_f32_i32_e32 v26, v26
	v_cvt_f32_i32_e32 v28, v28
	v_lshl_add_u64 v[36:37], s[16:17], 0, v[36:37]
	v_cvt_f32_i32_e32 v25, v25
	v_cvt_f32_i32_e32 v23, v23
	v_cvt_f32_i32_e32 v22, v22
	v_cvt_f32_i32_e32 v24, v24
	v_cvt_f32_i32_e32 v21, v21
	v_cvt_f32_i32_e32 v19, v19
	v_cvt_f32_i32_e32 v18, v18
	v_cvt_f32_i32_e32 v20, v20
	s_nop 0
	s_waitcnt vmcnt(13)
	v_pk_mul_f32 v[30:31], v[248:249], v[30:31] op_sel_hi:[0,1]
	v_pk_mul_f32 v[32:33], v[248:249], v[32:33] op_sel_hi:[0,1]
	s_nop 0
	s_waitcnt vmcnt(12)
	v_lshlrev_b32_e32 v44, 16, v250
	v_and_b32_e32 v45, 0xffff0000, v250
	v_lshlrev_b32_e32 v42, 16, v251
	v_and_b32_e32 v43, 0xffff0000, v251
	v_pk_fma_f32 v[42:43], v[152:153], v[32:33], v[42:43]
	v_pk_fma_f32 v[44:45], v[128:129], v[30:31], v[44:45]
	v_pk_mul_f32 v[26:27], v[248:249], v[26:27] op_sel_hi:[0,1]
	v_cvt_pk_bf16_f32 v48, v44, v45
	v_cvt_pk_bf16_f32 v49, v42, v43
	s_nop 0
	s_nop 0
	v_pk_mul_f32 v[28:29], v[248:249], v[28:29] op_sel_hi:[0,1]
	v_pk_mul_f32 v[22:23], v[248:249], v[22:23] op_sel_hi:[0,1]
	v_pk_mul_f32 v[24:25], v[248:249], v[24:25] op_sel_hi:[0,1]
	v_pk_mul_f32 v[18:19], v[248:249], v[18:19] op_sel_hi:[0,1]
	v_pk_mul_f32 v[20:21], v[248:249], v[20:21] op_sel_hi:[0,1]
	s_nop 0
	v_mul_f32_e32 v30, v192, v44
	v_mul_f32_e32 v31, v193, v45
	v_mul_f32_e32 v32, v194, v42
	v_mul_f32_e32 v33, v195, v43
	v_cvt_pk_bf16_f32 v52, v30, v31
	v_cvt_pk_bf16_f32 v53, v32, v33
	s_nop 0
	s_nop 0
	s_nop 0
	s_nop 0
	s_waitcnt vmcnt(11)
; __device__ __forceinline__ unsigned cvt_pk_bf16(float lo, float hi) { unsigned r; asm volatile("v_cvt_pk_bf16_f32 %0, %1, %2" : "=v"(r) : "v"(lo), "v"(hi)); return r; }
;     __device__ __forceinline__ void operator()(const f32x4 (&acc)[2][2][4][2], const Unit& u, int wr, int wc, int fr, int fq) const {
;     ...
;             for (int m = 0; m < 4; ++m) { const int row = row0 + ai * HALF + m * 16; const size_t ro = (size_t)row * ldc + col0; float ss = 0.f; const float rs = xs[row];
; #pragma unroll
;                 for (int bj = 0; bj < 2; ++bj)
; #pragma unroll
;                     for (int n = 0; n < 2; ++n) { const i32x4 ia = __builtin_bit_cast(i32x4, acc[ai][bj][m][n]);
;                         const f32x4 af = (f32x4){(float)ia[0], (float)ia[1], (float)ia[2], (float)ia[3]} * rs * cs[bj][n];
;                         f32x4 rv; if constexpr (RB16) { const u32x2 rb = *(const u32x2*)((const bf16_t*)R + ro + bj * HALF + n * 4); rv = (f32x4){__uint_as_float(rb.x << 16), __uint_as_float(rb.x & 0xffff0000u), __uint_as_float(rb.y << 16), __uint_as_float(rb.y & 0xffff0000u)}; }
;                         else rv = *(const f32x4*)((const float*)R + ro + bj * HALF + n * 4);
;                         const f32x4 v = af + rv; { u32x2 hb; hb.x = cvt_pk_bf16(v[0], v[1]); hb.y = cvt_pk_bf16(v[2], v[3]); *(u32x2*)(C + ro + bj * HALF + n * 4) = hb; }
;                         const f32x4 g = *(const f32x4*)(gain + col0 + bj * HALF + n * 4);
;                         u32x2 o; o.x = cvt_pk_bf16(v[0] * g[0], v[1] * g[1]); o.y = cvt_pk_bf16(v[2] * g[2], v[3] * g[3]); *(u32x2*)(HG + ro + bj * HALF + n * 4) = o;
;                         ss += (v[0] * v[0] + v[1] * v[1]) + (v[2] * v[2] + v[3] * v[3]); }
;                 ss += __shfl_xor(ss, 16); ss += __shfl_xor(ss, 32);
;                 if (fq == 0) SS[(size_t)row * 64 + u.pn * 4 + wc] = ss; }
	v_lshlrev_b32_e32 v30, 16, v244
	v_and_b32_e32 v31, 0xffff0000, v244
	v_lshlrev_b32_e32 v32, 16, v245
	v_and_b32_e32 v33, 0xffff0000, v245
	v_pk_fma_f32 v[32:33], v[124:125], v[28:29], v[32:33]
	v_pk_fma_f32 v[30:31], v[122:123], v[26:27], v[30:31]
	s_nop 0
	v_cvt_pk_bf16_f32 v50, v30, v31
	v_cvt_pk_bf16_f32 v51, v32, v33
	global_store_dwordx4 v[40:41], v[48:51], off
	s_nop 0
	s_nop 0
	v_mul_f32_e32 v26, v196, v30
	v_mul_f32_e32 v27, v197, v31
	v_mul_f32_e32 v28, v198, v32
	v_mul_f32_e32 v29, v199, v33
	v_cvt_pk_bf16_f32 v54, v26, v27
	v_cvt_pk_bf16_f32 v55, v28, v29
	s_nop 0
	s_nop 0
	global_store_dwordx4 v[36:37], v[52:55], off
	s_nop 0
	s_waitcnt vmcnt(12)
	v_lshlrev_b32_e32 v26, 16, v232
	v_and_b32_e32 v27, 0xffff0000, v232
	v_lshlrev_b32_e32 v28, 16, v233
	v_and_b32_e32 v29, 0xffff0000, v233
	v_pk_fma_f32 v[28:29], v[120:121], v[24:25], v[28:29]
	v_pk_fma_f32 v[26:27], v[118:119], v[22:23], v[26:27]
	s_nop 0
	v_cvt_pk_bf16_f32 v48, v26, v27
	v_cvt_pk_bf16_f32 v49, v28, v29
	s_nop 0
	s_nop 0
	s_nop 0
	v_mul_f32_e32 v22, v200, v26
	v_mul_f32_e32 v23, v201, v27
	v_mul_f32_e32 v24, v202, v28
	v_mul_f32_e32 v25, v203, v29
	v_cvt_pk_bf16_f32 v52, v22, v23
	v_cvt_pk_bf16_f32 v53, v24, v25
	s_nop 0
	s_nop 0
	s_nop 0
	s_nop 0
	s_waitcnt vmcnt(11)
	v_lshlrev_b32_e32 v22, 16, v234
	v_and_b32_e32 v23, 0xffff0000, v234
	v_lshlrev_b32_e32 v24, 16, v235
	v_and_b32_e32 v25, 0xffff0000, v235
	v_pk_fma_f32 v[24:25], v[116:117], v[20:21], v[24:25]
	v_pk_fma_f32 v[38:39], v[114:115], v[18:19], v[22:23]
	s_nop 0
	v_cvt_pk_bf16_f32 v50, v38, v39
	v_cvt_pk_bf16_f32 v51, v24, v25
	global_store_dwordx4 v[40:41], v[48:51], off offset:256
	s_nop 0
	v_mul_f32_e32 v18, v45, v45
	v_mul_f32_e32 v19, v43, v43
	v_fmac_f32_e32 v18, v44, v44
	v_fmac_f32_e32 v19, v42, v42
	v_add_f32_e32 v18, v18, v19
	v_mul_f32_e32 v19, v31, v31
	v_mul_f32_e32 v31, v33, v33
	v_fmac_f32_e32 v19, v30, v30
	v_fmac_f32_e32 v31, v32, v32
	v_add_f32_e32 v19, v19, v31
	v_add_f32_e32 v18, v18, v19
	v_mul_f32_e32 v19, v27, v27
	v_mul_f32_e32 v27, v29, v29
	v_fmac_f32_e32 v19, v26, v26
	v_fmac_f32_e32 v27, v28, v28
	v_add_f32_e32 v19, v19, v27
	v_add_f32_e32 v18, v18, v19
	v_mul_f32_e32 v19, v39, v39
	v_mul_f32_e32 v26, v25, v25
	v_fmac_f32_e32 v19, v38, v38
	v_fmac_f32_e32 v26, v24, v24
	v_add_f32_e32 v19, v19, v26
	v_add_f32_e32 v18, v18, v19
	ds_bpermute_b32 v19, v162, v18
	s_waitcnt lgkmcnt(0)
	v_add_f32_e32 v18, v18, v19
	ds_bpermute_b32 v19, v163, v18
	s_nop 0
	v_mul_f32_e32 v20, v204, v38
	v_mul_f32_e32 v21, v205, v39
	v_mul_f32_e32 v22, v206, v24
	v_mul_f32_e32 v23, v207, v25
	v_cvt_pk_bf16_f32 v54, v20, v21
	v_cvt_pk_bf16_f32 v55, v22, v23
	global_store_dwordx4 v[36:37], v[52:55], off offset:256
	s_and_saveexec_b64 s[50:51], s[4:5]
	s_cbranch_execz .LBB0_1956
	s_waitcnt lgkmcnt(0)
	v_add_f32_e32 v20, v18, v19
	v_lshlrev_b64 v[18:19], 8, v[34:35]
	v_lshl_add_u64 v[18:19], s[20:21], 0, v[18:19]
	v_lshl_add_u64 v[18:19], s[48:49], 2, v[18:19]
	s_lshl_b32 s10, s64, 2
	v_lshl_add_u64 v[18:19], v[18:19], 0, s[10:11]
	global_store_dword v[18:19], v20, off
; __device__ __forceinline__ unsigned cvt_pk_bf16(float lo, float hi) { unsigned r; asm volatile("v_cvt_pk_bf16_f32 %0, %1, %2" : "=v"(r) : "v"(lo), "v"(hi)); return r; }
;     __device__ __forceinline__ void operator()(const f32x4 (&acc)[2][2][4][2], const Unit& u, int wr, int wc, int fr, int fq) const {
;     ...
;             for (int m = 0; m < 4; ++m) { const int row = row0 + ai * HALF + m * 16; const size_t ro = (size_t)row * ldc + col0; float ss = 0.f; const float rs = xs[row];
; #pragma unroll
;                 for (int bj = 0; bj < 2; ++bj)
; #pragma unroll
;                     for (int n = 0; n < 2; ++n) { const i32x4 ia = __builtin_bit_cast(i32x4, acc[ai][bj][m][n]);
;                         const f32x4 af = (f32x4){(float)ia[0], (float)ia[1], (float)ia[2], (float)ia[3]} * rs * cs[bj][n];
;                         f32x4 rv; if constexpr (RB16) { const u32x2 rb = *(const u32x2*)((const bf16_t*)R + ro + bj * HALF + n * 4); rv = (f32x4){__uint_as_float(rb.x << 16), __uint_as_float(rb.x & 0xffff0000u), __uint_as_float(rb.y << 16), __uint_as_float(rb.y & 0xffff0000u)}; }
;                         else rv = *(const f32x4*)((const float*)R + ro + bj * HALF + n * 4);
;                         const f32x4 v = af + rv; { u32x2 hb; hb.x = cvt_pk_bf16(v[0], v[1]); hb.y = cvt_pk_bf16(v[2], v[3]); *(u32x2*)(C + ro + bj * HALF + n * 4) = hb; }
;                         const f32x4 g = *(const f32x4*)(gain + col0 + bj * HALF + n * 4);
;                         u32x2 o; o.x = cvt_pk_bf16(v[0] * g[0], v[1] * g[1]); o.y = cvt_pk_bf16(v[2] * g[2], v[3] * g[3]); *(u32x2*)(HG + ro + bj * HALF + n * 4) = o;
;                         ss += (v[0] * v[0] + v[1] * v[1]) + (v[2] * v[2] + v[3] * v[3]); }
;                 ss += __shfl_xor(ss, 16); ss += __shfl_xor(ss, 32);
;                 if (fq == 0) SS[(size_t)row * 64 + u.pn * 4 + wc] = ss; }
.LBB0_1956:
	s_or_b64 exec, exec, s[50:51]
	v_add_u32_e32 v18, 0xb0, v148
	s_waitcnt lgkmcnt(0)
	v_ashrrev_i32_e32 v19, 31, v18
	v_lshlrev_b64 v[20:21], 12, v[18:19]
	v_lshl_add_u64 v[20:21], v[20:21], 0, v[146:147]
	v_lshlrev_b64 v[20:21], 1, v[20:21]
	v_lshl_add_u64 v[24:25], s[14:15], 0, v[20:21]
	s_nop 0
	s_nop 0
	v_cvt_f32_i32_e32 v17, v17
	v_cvt_f32_i32_e32 v15, v15
	v_cvt_f32_i32_e32 v14, v14
	v_cvt_f32_i32_e32 v16, v16
	v_cvt_f32_i32_e32 v13, v13
	v_cvt_f32_i32_e32 v11, v11
	v_cvt_f32_i32_e32 v10, v10
	v_cvt_f32_i32_e32 v12, v12
	v_lshl_add_u64 v[20:21], s[16:17], 0, v[20:21]
	v_cvt_f32_i32_e32 v9, v9
	v_cvt_f32_i32_e32 v7, v7
	v_cvt_f32_i32_e32 v6, v6
	v_cvt_f32_i32_e32 v8, v8
	v_cvt_f32_i32_e32 v5, v5
	v_cvt_f32_i32_e32 v3, v3
	v_cvt_f32_i32_e32 v2, v2
	v_cvt_f32_i32_e32 v4, v4
	s_nop 0
	s_waitcnt vmcnt(8)
	v_pk_mul_f32 v[14:15], v[246:247], v[14:15] op_sel_hi:[0,1]
	v_pk_mul_f32 v[16:17], v[246:247], v[16:17] op_sel_hi:[0,1]
	s_nop 0
	s_waitcnt vmcnt(7)
	v_lshlrev_b32_e32 v28, 16, v240
	v_and_b32_e32 v29, 0xffff0000, v240
	v_lshlrev_b32_e32 v26, 16, v241
	v_and_b32_e32 v27, 0xffff0000, v241
	v_pk_fma_f32 v[26:27], v[152:153], v[16:17], v[26:27]
	v_pk_fma_f32 v[28:29], v[128:129], v[14:15], v[28:29]
	v_pk_mul_f32 v[10:11], v[246:247], v[10:11] op_sel_hi:[0,1]
	v_cvt_pk_bf16_f32 v32, v28, v29
	v_cvt_pk_bf16_f32 v33, v26, v27
	s_nop 0
	s_nop 0
	v_pk_mul_f32 v[12:13], v[246:247], v[12:13] op_sel_hi:[0,1]
	v_pk_mul_f32 v[6:7], v[246:247], v[6:7] op_sel_hi:[0,1]
	v_pk_mul_f32 v[8:9], v[246:247], v[8:9] op_sel_hi:[0,1]
	v_pk_mul_f32 v[2:3], v[246:247], v[2:3] op_sel_hi:[0,1]
	v_pk_mul_f32 v[4:5], v[246:247], v[4:5] op_sel_hi:[0,1]
	s_nop 0
	v_mul_f32_e32 v14, v192, v28
	v_mul_f32_e32 v15, v193, v29
	v_mul_f32_e32 v16, v194, v26
	v_mul_f32_e32 v17, v195, v27
	v_cvt_pk_bf16_f32 v36, v14, v15
	v_cvt_pk_bf16_f32 v37, v16, v17
	s_nop 0
	s_nop 0
	s_nop 0
	s_nop 0
	s_waitcnt vmcnt(6)
	v_lshlrev_b32_e32 v14, 16, v242
	v_and_b32_e32 v15, 0xffff0000, v242
	v_lshlrev_b32_e32 v16, 16, v243
	v_and_b32_e32 v17, 0xffff0000, v243
	v_pk_fma_f32 v[16:17], v[124:125], v[12:13], v[16:17]
	v_pk_fma_f32 v[14:15], v[122:123], v[10:11], v[14:15]
	s_nop 0
	v_cvt_pk_bf16_f32 v34, v14, v15
	v_cvt_pk_bf16_f32 v35, v16, v17
	global_store_dwordx4 v[24:25], v[32:35], off
	s_nop 0
	s_nop 0
	v_mul_f32_e32 v10, v196, v14
	v_mul_f32_e32 v11, v197, v15
	v_mul_f32_e32 v12, v198, v16
	v_mul_f32_e32 v13, v199, v17
	v_cvt_pk_bf16_f32 v38, v10, v11
	v_cvt_pk_bf16_f32 v39, v12, v13
	s_nop 0
	s_nop 0
	global_store_dwordx4 v[20:21], v[36:39], off
	s_nop 0
	s_waitcnt vmcnt(7)
	v_lshlrev_b32_e32 v10, 16, v236
	v_and_b32_e32 v11, 0xffff0000, v236
	v_lshlrev_b32_e32 v12, 16, v237
	v_and_b32_e32 v13, 0xffff0000, v237
	v_pk_fma_f32 v[12:13], v[120:121], v[8:9], v[12:13]
	v_pk_fma_f32 v[10:11], v[118:119], v[6:7], v[10:11]
	s_nop 0
	v_cvt_pk_bf16_f32 v32, v10, v11
	v_cvt_pk_bf16_f32 v33, v12, v13
	s_nop 0
	s_nop 0
	s_nop 0
	v_mul_f32_e32 v6, v200, v10
	v_mul_f32_e32 v7, v201, v11
	v_mul_f32_e32 v8, v202, v12
	v_mul_f32_e32 v9, v203, v13
	v_cvt_pk_bf16_f32 v36, v6, v7
	v_cvt_pk_bf16_f32 v37, v8, v9
	s_nop 0
	s_nop 0
	s_nop 0
	s_nop 0
	s_waitcnt vmcnt(6)
	v_lshlrev_b32_e32 v6, 16, v238
	v_and_b32_e32 v7, 0xffff0000, v238
	v_lshlrev_b32_e32 v8, 16, v239
	v_and_b32_e32 v9, 0xffff0000, v239
	v_pk_fma_f32 v[8:9], v[116:117], v[4:5], v[8:9]
	v_pk_fma_f32 v[22:23], v[114:115], v[2:3], v[6:7]
	s_nop 0
	v_cvt_pk_bf16_f32 v34, v22, v23
	v_cvt_pk_bf16_f32 v35, v8, v9
	global_store_dwordx4 v[24:25], v[32:35], off offset:256
	s_nop 0
	v_mul_f32_e32 v2, v29, v29
	v_mul_f32_e32 v3, v27, v27
	v_fmac_f32_e32 v2, v28, v28
	v_fmac_f32_e32 v3, v26, v26
	v_add_f32_e32 v2, v2, v3
	v_mul_f32_e32 v3, v15, v15
	v_mul_f32_e32 v15, v17, v17
	v_fmac_f32_e32 v3, v14, v14
	v_fmac_f32_e32 v15, v16, v16
	v_add_f32_e32 v3, v3, v15
	v_add_f32_e32 v2, v2, v3
	v_mul_f32_e32 v3, v11, v11
	v_mul_f32_e32 v11, v13, v13
	v_fmac_f32_e32 v3, v10, v10
	v_fmac_f32_e32 v11, v12, v12
	v_add_f32_e32 v3, v3, v11
	v_add_f32_e32 v2, v2, v3
	v_mul_f32_e32 v3, v23, v23
	v_mul_f32_e32 v10, v9, v9
	v_fmac_f32_e32 v3, v22, v22
	v_fmac_f32_e32 v10, v8, v8
	v_add_f32_e32 v3, v3, v10
	v_add_f32_e32 v2, v2, v3
	ds_bpermute_b32 v3, v162, v2
	s_waitcnt lgkmcnt(0)
	v_add_f32_e32 v2, v2, v3
	ds_bpermute_b32 v3, v163, v2
	s_nop 0
	v_mul_f32_e32 v4, v204, v22
	v_mul_f32_e32 v5, v205, v23
	v_mul_f32_e32 v6, v206, v8
	v_mul_f32_e32 v7, v207, v9
	v_cvt_pk_bf16_f32 v38, v4, v5
	v_cvt_pk_bf16_f32 v39, v6, v7
	global_store_dwordx4 v[20:21], v[36:39], off offset:256
	s_and_saveexec_b64 s[50:51], s[4:5]
	s_cbranch_execz .LBB0_1958
	s_waitcnt lgkmcnt(0)
	v_add_f32_e32 v4, v2, v3
	v_lshlrev_b64 v[2:3], 8, v[18:19]
	v_lshl_add_u64 v[2:3], s[20:21], 0, v[2:3]
	v_lshl_add_u64 v[2:3], s[48:49], 2, v[2:3]
	s_lshl_b32 s10, s64, 2
	v_lshl_add_u64 v[2:3], v[2:3], 0, s[10:11]
	global_store_dword v[2:3], v4, off
